# v99 + MFMA issue prioritised in the attention tile loops: s_setprio 1 around each run of MFMAs (27 runs in the 8 loops), back to 0 for the softmax VALU
# baseline (speedup 1.0000x reference)
.LBB0_497:
	v_lshl_add_u64 v[140:141], v[200:201], 0, s[74:75]
	v_add_co_u32_e32 v64, vcc, s67, v140
	v_lshl_add_u64 v[138:139], v[198:199], 0, s[74:75]
	s_nop 0
	v_addc_co_u32_e32 v65, vcc, 0, v141, vcc
	v_add_co_u32_e32 v66, vcc, s67, v138
	v_lshl_add_u64 v[136:137], v[196:197], 0, s[74:75]
	s_nop 0
	v_addc_co_u32_e32 v67, vcc, 0, v139, vcc
	global_load_dwordx4 v[178:181], v[64:65], off offset:1024
	global_load_dwordx4 v[182:185], v[66:67], off offset:2048
	v_add_co_u32_e32 v64, vcc, s67, v136
	s_nop 1
	v_addc_co_u32_e32 v65, vcc, 0, v137, vcc
	global_load_dwordx4 v[186:189], v[64:65], off offset:2048
	v_add_u32_e32 v142, v206, v207
	v_add_u32_e32 v143, v206, v208
	v_add_u32_e32 v144, v206, v209
	v_add_u32_e32 v145, v206, v210
	ds_read_b128 v[80:83], v142 offset:32768
	ds_read_b128 v[98:101], v142 offset:40960
	ds_read_b128 v[132:135], v143 offset:32768
	ds_read_b128 v[76:79], v143 offset:40960
	ds_read_b128 v[128:131], v144 offset:32768
	ds_read_b128 v[68:71], v144 offset:40960
	ds_read_b128 v[72:75], v145 offset:32768
	ds_read_b128 v[64:67], v145 offset:40960
	s_cmp_eq_u32 s74, 0
	s_cbranch_scc1 .LBB0_499
	ds_read_b64_tr_b16 v[84:85], v217 offset:0
	ds_read_b64_tr_b16 v[86:87], v217 offset:0x800
	ds_read_b64_tr_b16 v[88:89], v217 offset:0x1000
	ds_read_b64_tr_b16 v[90:91], v217 offset:0x1800
	ds_read_b64_tr_b16 v[92:93], v217 offset:0x2000
	ds_read_b64_tr_b16 v[94:95], v217 offset:0x2800
	ds_read_b64_tr_b16 v[102:103], v217 offset:0x3000
	ds_read_b64_tr_b16 v[104:105], v217 offset:0x3800
	s_waitcnt lgkmcnt(0)
	s_nop 0
	s_setprio 1
	v_mfma_f32_32x32x16_bf16 v[0:15], v[112:115], v[84:87], v[0:15]
	ds_read_b64_tr_b16 v[84:85], v217 offset:0x200
	ds_read_b64_tr_b16 v[86:87], v217 offset:0xa00
	v_mfma_f32_32x32x16_bf16 v[0:15], v[116:119], v[88:91], v[0:15]
	ds_read_b64_tr_b16 v[88:89], v217 offset:0x1200
	ds_read_b64_tr_b16 v[90:91], v217 offset:0x1a00
	v_mfma_f32_32x32x16_bf16 v[0:15], v[124:127], v[92:95], v[0:15]
	ds_read_b64_tr_b16 v[92:93], v217 offset:0x2200
	ds_read_b64_tr_b16 v[94:95], v217 offset:0x2a00
	v_mfma_f32_32x32x16_bf16 v[0:15], v[120:123], v[102:105], v[0:15]
	ds_read_b64_tr_b16 v[102:103], v217 offset:0x3200
	ds_read_b64_tr_b16 v[104:105], v217 offset:0x3a00
	s_waitcnt lgkmcnt(0)
	v_mfma_f32_32x32x16_bf16 v[16:31], v[112:115], v[84:87], v[16:31]
	ds_read_b64_tr_b16 v[84:85], v217 offset:0x400
	ds_read_b64_tr_b16 v[86:87], v217 offset:0xc00
	v_mfma_f32_32x32x16_bf16 v[16:31], v[116:119], v[88:91], v[16:31]
	ds_read_b64_tr_b16 v[88:89], v217 offset:0x1400
	ds_read_b64_tr_b16 v[90:91], v217 offset:0x1c00
	v_mfma_f32_32x32x16_bf16 v[16:31], v[124:127], v[92:95], v[16:31]
	ds_read_b64_tr_b16 v[92:93], v217 offset:0x2400
	ds_read_b64_tr_b16 v[94:95], v217 offset:0x2c00
	v_mfma_f32_32x32x16_bf16 v[16:31], v[120:123], v[102:105], v[16:31]
	ds_read_b64_tr_b16 v[102:103], v217 offset:0x3400
	ds_read_b64_tr_b16 v[104:105], v217 offset:0x3c00
	s_waitcnt lgkmcnt(0)
	v_mfma_f32_32x32x16_bf16 v[32:47], v[112:115], v[84:87], v[32:47]
	ds_read_b64_tr_b16 v[84:85], v217 offset:0x600
	ds_read_b64_tr_b16 v[86:87], v217 offset:0xe00
	v_mfma_f32_32x32x16_bf16 v[32:47], v[116:119], v[88:91], v[32:47]
	ds_read_b64_tr_b16 v[88:89], v217 offset:0x1600
	ds_read_b64_tr_b16 v[90:91], v217 offset:0x1e00
	v_mfma_f32_32x32x16_bf16 v[32:47], v[124:127], v[92:95], v[32:47]
	ds_read_b64_tr_b16 v[92:93], v217 offset:0x2600
	ds_read_b64_tr_b16 v[94:95], v217 offset:0x2e00
	v_mfma_f32_32x32x16_bf16 v[32:47], v[120:123], v[102:105], v[32:47]
	ds_read_b64_tr_b16 v[102:103], v217 offset:0x3600
	ds_read_b64_tr_b16 v[104:105], v217 offset:0x3e00
	s_waitcnt lgkmcnt(0)
	v_mfma_f32_32x32x16_bf16 v[48:63], v[112:115], v[84:87], v[48:63]
	v_mfma_f32_32x32x16_bf16 v[48:63], v[116:119], v[88:91], v[48:63]
	v_mfma_f32_32x32x16_bf16 v[48:63], v[124:127], v[92:95], v[48:63]
	v_mfma_f32_32x32x16_bf16 v[48:63], v[120:123], v[102:105], v[48:63]
	s_setprio 0
.LBB0_499:
	s_waitcnt lgkmcnt(7)
	s_setprio 1
	v_mfma_f32_32x32x16_bf16 v[82:97], v[80:83], v[162:165], 0
	s_waitcnt lgkmcnt(6)
	v_mfma_f32_32x32x16_bf16 v[98:113], v[98:101], v[162:165], 0
	s_waitcnt lgkmcnt(5)
	v_mfma_f32_32x32x16_bf16 v[82:97], v[132:135], v[166:169], v[82:97]
	s_waitcnt lgkmcnt(4)
	v_mfma_f32_32x32x16_bf16 v[98:113], v[76:79], v[166:169], v[98:113]
	s_waitcnt lgkmcnt(3)
	v_mfma_f32_32x32x16_bf16 v[82:97], v[128:131], v[170:173], v[82:97]
	s_waitcnt lgkmcnt(2)
	v_mfma_f32_32x32x16_bf16 v[98:113], v[68:71], v[170:173], v[98:113]
	s_waitcnt lgkmcnt(1)
	v_mfma_f32_32x32x16_bf16 v[82:97], v[72:75], v[174:177], v[82:97]
	s_waitcnt lgkmcnt(0)
	v_mfma_f32_32x32x16_bf16 v[98:113], v[64:67], v[174:177], v[98:113]
	s_setprio 0
	s_barrier
	v_cndmask_b32_e64 v64, 0, 1, s[40:41]
	v_cmp_ne_u32_e64 s[42:43], 1, v64
	s_andn2_b64 vcc, exec, s[40:41]
	s_mov_b64 s[2:3], -1
	s_cbranch_vccnz .LBB0_503
	s_nop 3
	v_exp_f32_e32 v64, v82
	v_exp_f32_e32 v65, v83
	v_exp_f32_e32 v66, v84
	v_exp_f32_e32 v67, v85
	v_exp_f32_e32 v68, v86
	v_exp_f32_e32 v69, v87
	v_exp_f32_e32 v70, v88
	v_exp_f32_e32 v71, v89
	v_exp_f32_e32 v72, v90
	v_exp_f32_e32 v73, v91
	v_exp_f32_e32 v74, v92
	v_exp_f32_e32 v75, v93
	v_exp_f32_e32 v76, v94
	v_exp_f32_e32 v77, v95
	v_exp_f32_e32 v78, v96
	s_cbranch_execz .LBB0_504

.LBB0_509:
	ds_read_b128 v[112:115], v142 offset:49152
	ds_read_b128 v[128:131], v142 offset:57344
	ds_read_b128 v[146:149], v143 offset:49152
	ds_read_b128 v[150:153], v143 offset:57344
	ds_read_b128 v[154:157], v144 offset:49152
	ds_read_b128 v[218:221], v144 offset:57344
	ds_read_b128 v[222:225], v145 offset:49152
	ds_read_b128 v[226:229], v145 offset:57344
	ds_read_b64_tr_b16 v[116:117], v212 offset:0
	ds_read_b64_tr_b16 v[118:119], v212 offset:0x800
	ds_read_b64_tr_b16 v[120:121], v212 offset:0x1000
	ds_read_b64_tr_b16 v[122:123], v212 offset:0x1800
	ds_read_b64_tr_b16 v[124:125], v212 offset:0x2000
	ds_read_b64_tr_b16 v[126:127], v212 offset:0x2800
	ds_read_b64_tr_b16 v[132:133], v212 offset:0x3000
	ds_read_b64_tr_b16 v[134:135], v212 offset:0x3800
	s_waitcnt lgkmcnt(0)
	s_nop 0
	s_setprio 1
	v_mfma_f32_32x32x16_bf16 v[0:15], v[96:99], v[116:119], v[0:15]
	ds_read_b64_tr_b16 v[116:117], v212 offset:0x200
	ds_read_b64_tr_b16 v[118:119], v212 offset:0xa00
	v_mfma_f32_32x32x16_bf16 v[0:15], v[100:103], v[120:123], v[0:15]
	ds_read_b64_tr_b16 v[120:121], v212 offset:0x1200
	ds_read_b64_tr_b16 v[122:123], v212 offset:0x1a00
	v_mfma_f32_32x32x16_bf16 v[0:15], v[104:107], v[124:127], v[0:15]
	ds_read_b64_tr_b16 v[124:125], v212 offset:0x2200
	ds_read_b64_tr_b16 v[126:127], v212 offset:0x2a00
	v_mfma_f32_32x32x16_bf16 v[0:15], v[108:111], v[132:135], v[0:15]
	ds_read_b64_tr_b16 v[132:133], v212 offset:0x3200
	ds_read_b64_tr_b16 v[134:135], v212 offset:0x3a00
	s_waitcnt lgkmcnt(0)
	v_mfma_f32_32x32x16_bf16 v[16:31], v[96:99], v[116:119], v[16:31]
	ds_read_b64_tr_b16 v[116:117], v212 offset:0x400
	ds_read_b64_tr_b16 v[118:119], v212 offset:0xc00
	v_mfma_f32_32x32x16_bf16 v[16:31], v[100:103], v[120:123], v[16:31]
	ds_read_b64_tr_b16 v[120:121], v212 offset:0x1400
	ds_read_b64_tr_b16 v[122:123], v212 offset:0x1c00
	v_mfma_f32_32x32x16_bf16 v[16:31], v[104:107], v[124:127], v[16:31]
	ds_read_b64_tr_b16 v[124:125], v212 offset:0x2400
	ds_read_b64_tr_b16 v[126:127], v212 offset:0x2c00
	v_mfma_f32_32x32x16_bf16 v[16:31], v[108:111], v[132:135], v[16:31]
	ds_read_b64_tr_b16 v[132:133], v212 offset:0x3400
	ds_read_b64_tr_b16 v[134:135], v212 offset:0x3c00
	s_waitcnt lgkmcnt(0)
	v_mfma_f32_32x32x16_bf16 v[32:47], v[96:99], v[116:119], v[32:47]
	ds_read_b64_tr_b16 v[116:117], v212 offset:0x600
	ds_read_b64_tr_b16 v[118:119], v212 offset:0xe00
	v_mfma_f32_32x32x16_bf16 v[32:47], v[100:103], v[120:123], v[32:47]
	ds_read_b64_tr_b16 v[120:121], v212 offset:0x1600
	ds_read_b64_tr_b16 v[122:123], v212 offset:0x1e00
	v_mfma_f32_32x32x16_bf16 v[32:47], v[104:107], v[124:127], v[32:47]
	ds_read_b64_tr_b16 v[124:125], v212 offset:0x2600
	ds_read_b64_tr_b16 v[126:127], v212 offset:0x2e00
	v_mfma_f32_32x32x16_bf16 v[32:47], v[108:111], v[132:135], v[32:47]
	ds_read_b64_tr_b16 v[132:133], v212 offset:0x3600
	ds_read_b64_tr_b16 v[134:135], v212 offset:0x3e00
	s_waitcnt lgkmcnt(0)
	v_mfma_f32_32x32x16_bf16 v[48:63], v[96:99], v[116:119], v[48:63]
	v_mfma_f32_32x32x16_bf16 v[48:63], v[100:103], v[120:123], v[48:63]
	v_mfma_f32_32x32x16_bf16 v[48:63], v[104:107], v[124:127], v[48:63]
	v_mfma_f32_32x32x16_bf16 v[48:63], v[108:111], v[132:135], v[48:63]
	s_waitcnt lgkmcnt(7)
	v_mfma_f32_32x32x16_bf16 v[112:127], v[112:115], v[162:165], 0
	s_waitcnt lgkmcnt(6)
	v_mfma_f32_32x32x16_bf16 v[128:143], v[128:131], v[162:165], 0
	s_waitcnt lgkmcnt(5)
	v_mfma_f32_32x32x16_bf16 v[112:127], v[146:149], v[166:169], v[112:127]
	s_waitcnt lgkmcnt(4)
	v_mfma_f32_32x32x16_bf16 v[128:143], v[150:153], v[166:169], v[128:143]
	s_waitcnt lgkmcnt(3)
	v_mfma_f32_32x32x16_bf16 v[112:127], v[154:157], v[170:173], v[112:127]
	s_waitcnt lgkmcnt(2)
	v_mfma_f32_32x32x16_bf16 v[128:143], v[218:221], v[170:173], v[128:143]
	s_waitcnt lgkmcnt(1)
	v_mfma_f32_32x32x16_bf16 v[112:127], v[222:225], v[174:177], v[112:127]
	s_waitcnt lgkmcnt(0)
	v_mfma_f32_32x32x16_bf16 v[128:143], v[226:229], v[174:177], v[128:143]
	s_setprio 0
	s_barrier
	s_and_b64 vcc, exec, s[42:43]
	s_mov_b64 s[58:59], -1
	s_cbranch_vccnz .LBB0_513
	s_nop 5
	v_exp_f32_e32 v96, v112
	v_exp_f32_e32 v97, v113
	v_exp_f32_e32 v98, v114
	v_exp_f32_e32 v99, v115
	v_exp_f32_e32 v100, v116
	v_exp_f32_e32 v101, v117
	v_exp_f32_e32 v102, v118
	v_exp_f32_e32 v103, v119
	v_exp_f32_e32 v104, v120
	v_exp_f32_e32 v105, v121
	v_exp_f32_e32 v106, v122
	v_exp_f32_e32 v107, v123
	v_exp_f32_e32 v108, v124
	v_exp_f32_e32 v109, v125
	v_exp_f32_e32 v110, v126
	s_cbranch_execz .LBB0_514

.LBB0_523:
	v_lshl_add_u64 v[132:133], s[74:75], 0, v[192:193]
	v_add_co_u32_e32 v64, vcc, s67, v132
	v_lshl_add_u64 v[130:131], s[74:75], 0, v[194:195]
	s_nop 0
	v_addc_co_u32_e32 v65, vcc, 0, v133, vcc
	v_add_co_u32_e32 v66, vcc, s67, v130
	v_lshl_add_u64 v[128:129], s[74:75], 0, v[160:161]
	s_nop 0
	v_addc_co_u32_e32 v67, vcc, 0, v131, vcc
	global_load_dwordx4 v[146:149], v[64:65], off offset:1024
	global_load_dwordx4 v[150:153], v[66:67], off offset:2048
	v_add_co_u32_e32 v64, vcc, s67, v128
	s_nop 1
	v_addc_co_u32_e32 v65, vcc, 0, v129, vcc
	global_load_dwordx4 v[154:157], v[64:65], off offset:2048
	v_add_u32_e32 v134, v206, v207
	v_add_u32_e32 v135, v206, v208
	v_add_u32_e32 v136, v206, v209
	v_add_u32_e32 v137, v206, v210
	ds_read_b128 v[64:67], v134 offset:32768
	ds_read_b128 v[68:71], v134 offset:40960
	ds_read_b128 v[72:75], v135 offset:32768
	ds_read_b128 v[76:79], v135 offset:40960
	ds_read_b128 v[80:83], v136 offset:32768
	ds_read_b128 v[84:87], v136 offset:40960
	ds_read_b128 v[88:91], v137 offset:32768
	ds_read_b128 v[92:95], v137 offset:40960
	s_waitcnt lgkmcnt(7)
	s_setprio 1
	v_mfma_f32_32x32x16_bf16 v[112:127], v[64:67], v[162:165], 0
	s_waitcnt lgkmcnt(6)
	v_mfma_f32_32x32x16_bf16 v[96:111], v[68:71], v[162:165], 0
	s_waitcnt lgkmcnt(5)
	v_mfma_f32_32x32x16_bf16 v[112:127], v[72:75], v[166:169], v[112:127]
	s_waitcnt lgkmcnt(4)
	v_mfma_f32_32x32x16_bf16 v[96:111], v[76:79], v[166:169], v[96:111]
	s_waitcnt lgkmcnt(3)
	v_mfma_f32_32x32x16_bf16 v[112:127], v[80:83], v[170:173], v[112:127]
	s_waitcnt lgkmcnt(2)
	v_mfma_f32_32x32x16_bf16 v[96:111], v[84:87], v[170:173], v[96:111]
	s_waitcnt lgkmcnt(1)
	v_mfma_f32_32x32x16_bf16 v[112:127], v[88:91], v[174:177], v[112:127]
	s_waitcnt lgkmcnt(0)
	v_mfma_f32_32x32x16_bf16 v[96:111], v[92:95], v[174:177], v[96:111]
	s_setprio 0
	v_cndmask_b32_e64 v64, 0, 1, s[40:41]
	v_cmp_ne_u32_e64 s[42:43], 1, v64
	s_andn2_b64 vcc, exec, s[40:41]
	s_mov_b64 s[2:3], -1
	s_cbranch_vccnz .LBB0_527
	s_nop 4
	v_exp_f32_e32 v64, v112
	v_exp_f32_e32 v65, v113
	v_exp_f32_e32 v66, v114
	v_exp_f32_e32 v67, v115
	v_exp_f32_e32 v68, v116
	v_exp_f32_e32 v69, v117
	v_exp_f32_e32 v70, v118
	v_exp_f32_e32 v71, v119
	v_exp_f32_e32 v72, v120
	v_exp_f32_e32 v73, v121
	v_exp_f32_e32 v74, v122
	v_exp_f32_e32 v75, v123
	v_exp_f32_e32 v76, v124
	v_exp_f32_e32 v77, v125
	v_exp_f32_e32 v78, v126
	s_cbranch_execz .LBB0_528

.LBB0_531:
	v_exp_f32_e32 v79, v127
	v_exp_f32_e32 v95, v111
	v_cvt_pk_bf16_f32 v96, v64, v65
	v_cvt_pk_bf16_f32 v97, v66, v67
	v_cvt_pk_bf16_f32 v98, v68, v69
	v_cvt_pk_bf16_f32 v99, v70, v71
	v_cvt_pk_bf16_f32 v100, v72, v73
	v_cvt_pk_bf16_f32 v101, v74, v75
	v_cvt_pk_bf16_f32 v102, v76, v77
	v_cvt_pk_bf16_f32 v103, v78, v79
	v_cvt_pk_bf16_f32 v104, v80, v81
	v_cvt_pk_bf16_f32 v105, v82, v83
	v_cvt_pk_bf16_f32 v106, v84, v85
	v_cvt_pk_bf16_f32 v107, v86, v87
	v_cvt_pk_bf16_f32 v108, v88, v89
	v_cvt_pk_bf16_f32 v109, v90, v91
	v_cvt_pk_bf16_f32 v110, v92, v93
	v_cvt_pk_bf16_f32 v111, v94, v95
	v_permlane32_swap_b32_e32 v96, v98
	v_permlane32_swap_b32_e32 v97, v99
	v_permlane32_swap_b32_e32 v100, v102
	v_permlane32_swap_b32_e32 v101, v103
	v_permlane32_swap_b32_e32 v104, v106
	v_permlane32_swap_b32_e32 v105, v107
	v_permlane32_swap_b32_e32 v108, v110
	v_permlane32_swap_b32_e32 v109, v111
	s_barrier
	ds_read_b64_tr_b16 v[112:113], v212 offset:0
	ds_read_b64_tr_b16 v[114:115], v212 offset:0x800
	ds_read_b64_tr_b16 v[116:117], v212 offset:0x1000
	ds_read_b64_tr_b16 v[118:119], v212 offset:0x1800
	ds_read_b64_tr_b16 v[120:121], v212 offset:0x2000
	ds_read_b64_tr_b16 v[122:123], v212 offset:0x2800
	ds_read_b64_tr_b16 v[124:125], v212 offset:0x3000
	ds_read_b64_tr_b16 v[126:127], v212 offset:0x3800
	s_waitcnt lgkmcnt(0)
	s_nop 0
	s_setprio 1
	v_mfma_f32_32x32x16_bf16 v[0:15], v[96:99], v[112:115], v[0:15]
	ds_read_b64_tr_b16 v[112:113], v212 offset:0x200
	ds_read_b64_tr_b16 v[114:115], v212 offset:0xa00
	v_mfma_f32_32x32x16_bf16 v[0:15], v[100:103], v[116:119], v[0:15]
	ds_read_b64_tr_b16 v[116:117], v212 offset:0x1200
	ds_read_b64_tr_b16 v[118:119], v212 offset:0x1a00
	v_mfma_f32_32x32x16_bf16 v[0:15], v[104:107], v[120:123], v[0:15]
	ds_read_b64_tr_b16 v[120:121], v212 offset:0x2200
	ds_read_b64_tr_b16 v[122:123], v212 offset:0x2a00
	v_mfma_f32_32x32x16_bf16 v[0:15], v[108:111], v[124:127], v[0:15]
	ds_read_b64_tr_b16 v[124:125], v212 offset:0x3200
	ds_read_b64_tr_b16 v[126:127], v212 offset:0x3a00
	s_waitcnt lgkmcnt(0)
	v_mfma_f32_32x32x16_bf16 v[16:31], v[96:99], v[112:115], v[16:31]
	ds_read_b64_tr_b16 v[112:113], v212 offset:0x400
	ds_read_b64_tr_b16 v[114:115], v212 offset:0xc00
	v_mfma_f32_32x32x16_bf16 v[16:31], v[100:103], v[116:119], v[16:31]
	ds_read_b64_tr_b16 v[116:117], v212 offset:0x1400
	ds_read_b64_tr_b16 v[118:119], v212 offset:0x1c00
	v_mfma_f32_32x32x16_bf16 v[16:31], v[104:107], v[120:123], v[16:31]
	ds_read_b64_tr_b16 v[120:121], v212 offset:0x2400
	ds_read_b64_tr_b16 v[122:123], v212 offset:0x2c00
	v_mfma_f32_32x32x16_bf16 v[16:31], v[108:111], v[124:127], v[16:31]
	ds_read_b64_tr_b16 v[124:125], v212 offset:0x3400
	ds_read_b64_tr_b16 v[126:127], v212 offset:0x3c00
	s_waitcnt lgkmcnt(0)
	v_mfma_f32_32x32x16_bf16 v[32:47], v[96:99], v[112:115], v[32:47]
	ds_read_b64_tr_b16 v[112:113], v212 offset:0x600
	ds_read_b64_tr_b16 v[114:115], v212 offset:0xe00
	v_mfma_f32_32x32x16_bf16 v[32:47], v[100:103], v[116:119], v[32:47]
	ds_read_b64_tr_b16 v[116:117], v212 offset:0x1600
	ds_read_b64_tr_b16 v[118:119], v212 offset:0x1e00
	v_mfma_f32_32x32x16_bf16 v[32:47], v[104:107], v[120:123], v[32:47]
	ds_read_b64_tr_b16 v[120:121], v212 offset:0x2600
	ds_read_b64_tr_b16 v[122:123], v212 offset:0x2e00
	v_mfma_f32_32x32x16_bf16 v[32:47], v[108:111], v[124:127], v[32:47]
	ds_read_b64_tr_b16 v[124:125], v212 offset:0x3600
	ds_read_b64_tr_b16 v[126:127], v212 offset:0x3e00
	s_waitcnt lgkmcnt(0)
	v_mfma_f32_32x32x16_bf16 v[48:63], v[96:99], v[112:115], v[48:63]
	s_setprio 0
	s_cmp_lt_u32 s63, 30
	s_waitcnt vmcnt(0)
	s_cselect_b64 s[22:23], -1, 0
	s_cmp_gt_u32 s63, 29
	s_cselect_b64 s[2:3], -1, 0
	s_and_b64 vcc, exec, s[2:3]
	s_waitcnt vmcnt(2)
	ds_write_b128 v211, v[146:149] offset:49152
	s_waitcnt vmcnt(1)
	ds_write_b128 v213, v[150:153] offset:16384
	s_waitcnt vmcnt(0)
	ds_write_b128 v214, v[154:157] offset:16384
	v_mfma_f32_32x32x16_bf16 v[48:63], v[100:103], v[116:119], v[48:63]
	s_waitcnt lgkmcnt(0)
	s_barrier
	v_mfma_f32_32x32x16_bf16 v[48:63], v[104:107], v[120:123], v[48:63]
	v_mfma_f32_32x32x16_bf16 v[48:63], v[108:111], v[124:127], v[48:63]
	s_cbranch_vccnz .LBB0_533
	v_add_co_u32_e32 v96, vcc, 0x64d0000, v132
	s_nop 1
	v_addc_co_u32_e32 v97, vcc, 0, v133, vcc
	v_add_co_u32_e32 v98, vcc, 0x64d0000, v130
	s_nop 1
	v_addc_co_u32_e32 v99, vcc, 0, v131, vcc
	global_load_dwordx4 v[146:149], v[96:97], off offset:1024
	global_load_dwordx4 v[150:153], v[98:99], off offset:2048
	v_add_co_u32_e32 v96, vcc, 0x64d0000, v128
	s_nop 1
	v_addc_co_u32_e32 v97, vcc, 0, v129, vcc
	global_load_dwordx4 v[154:157], v[96:97], off offset:2048
.LBB0_533:
	ds_read_b128 v[96:99], v134 offset:49152
	ds_read_b128 v[100:103], v134 offset:57344
	ds_read_b128 v[104:107], v135 offset:49152
	ds_read_b128 v[108:111], v135 offset:57344
	ds_read_b128 v[178:181], v136 offset:49152
	ds_read_b128 v[182:185], v136 offset:57344
	ds_read_b128 v[186:189], v137 offset:49152
	ds_read_b128 v[196:199], v137 offset:57344
	s_waitcnt lgkmcnt(7)
	s_setprio 1
	v_mfma_f32_32x32x16_bf16 v[114:129], v[96:99], v[162:165], 0
	s_waitcnt lgkmcnt(6)
	v_mfma_f32_32x32x16_bf16 v[130:145], v[100:103], v[162:165], 0
	s_waitcnt lgkmcnt(5)
	v_mfma_f32_32x32x16_bf16 v[114:129], v[104:107], v[166:169], v[114:129]
	s_waitcnt lgkmcnt(4)
	v_mfma_f32_32x32x16_bf16 v[130:145], v[108:111], v[166:169], v[130:145]
	s_waitcnt lgkmcnt(3)
	v_mfma_f32_32x32x16_bf16 v[114:129], v[178:181], v[170:173], v[114:129]
	s_waitcnt lgkmcnt(2)
	v_mfma_f32_32x32x16_bf16 v[130:145], v[182:185], v[170:173], v[130:145]
	s_waitcnt lgkmcnt(1)
	v_mfma_f32_32x32x16_bf16 v[114:129], v[186:189], v[174:177], v[114:129]
	s_waitcnt lgkmcnt(0)
	v_mfma_f32_32x32x16_bf16 v[130:145], v[196:199], v[174:177], v[130:145]
	s_setprio 0
	s_and_b64 vcc, exec, s[42:43]
	s_mov_b64 s[58:59], -1
	s_cbranch_vccnz .LBB0_537
	s_nop 6
	v_exp_f32_e32 v96, v114
	v_exp_f32_e32 v97, v115
	v_exp_f32_e32 v98, v116
	v_exp_f32_e32 v99, v117
	v_exp_f32_e32 v100, v118
	v_exp_f32_e32 v101, v119
	v_exp_f32_e32 v102, v120
	v_exp_f32_e32 v103, v121
	v_exp_f32_e32 v104, v122
	v_exp_f32_e32 v105, v123
	v_exp_f32_e32 v106, v124
	v_exp_f32_e32 v107, v125
	v_exp_f32_e32 v108, v126
	v_exp_f32_e32 v109, v127
	v_exp_f32_e32 v110, v128
	s_cbranch_execz .LBB0_538

.LBB0_541:
	v_exp_f32_e32 v111, v129
	s_nop 0
	v_exp_f32_e32 v127, v145
	v_cvt_pk_bf16_f32 v128, v96, v97
	v_cvt_pk_bf16_f32 v129, v98, v99
	v_cvt_pk_bf16_f32 v130, v100, v101
	v_cvt_pk_bf16_f32 v131, v102, v103
	v_cvt_pk_bf16_f32 v132, v104, v105
	v_cvt_pk_bf16_f32 v133, v106, v107
	v_cvt_pk_bf16_f32 v134, v108, v109
	v_cvt_pk_bf16_f32 v135, v110, v111
	v_cvt_pk_bf16_f32 v136, v112, v113
	v_cvt_pk_bf16_f32 v137, v114, v115
	v_cvt_pk_bf16_f32 v138, v116, v117
	v_cvt_pk_bf16_f32 v139, v118, v119
	v_cvt_pk_bf16_f32 v140, v120, v121
	v_cvt_pk_bf16_f32 v141, v122, v123
	v_cvt_pk_bf16_f32 v142, v124, v125
	v_cvt_pk_bf16_f32 v143, v126, v127
	v_permlane32_swap_b32_e32 v128, v130
	v_permlane32_swap_b32_e32 v129, v131
	v_permlane32_swap_b32_e32 v132, v134
	v_permlane32_swap_b32_e32 v133, v135
	v_permlane32_swap_b32_e32 v136, v138
	v_permlane32_swap_b32_e32 v137, v139
	v_permlane32_swap_b32_e32 v140, v142
	v_permlane32_swap_b32_e32 v141, v143
	s_barrier
	ds_read_b64_tr_b16 v[178:179], v158 offset:0
	ds_read_b64_tr_b16 v[180:181], v158 offset:0x800
	ds_read_b64_tr_b16 v[182:183], v158 offset:0x1000
	ds_read_b64_tr_b16 v[184:185], v158 offset:0x1800
	ds_read_b64_tr_b16 v[186:187], v158 offset:0x2000
	ds_read_b64_tr_b16 v[188:189], v158 offset:0x2800
	ds_read_b64_tr_b16 v[196:197], v158 offset:0x3000
	ds_read_b64_tr_b16 v[198:199], v158 offset:0x3800
	s_waitcnt lgkmcnt(0)
	s_nop 0
	s_setprio 1
	v_mfma_f32_32x32x16_bf16 v[0:15], v[128:131], v[178:181], v[0:15]
	ds_read_b64_tr_b16 v[178:179], v158 offset:0x200
	ds_read_b64_tr_b16 v[180:181], v158 offset:0xa00
	v_mfma_f32_32x32x16_bf16 v[0:15], v[132:135], v[182:185], v[0:15]
	ds_read_b64_tr_b16 v[182:183], v158 offset:0x1200
	ds_read_b64_tr_b16 v[184:185], v158 offset:0x1a00
	v_mfma_f32_32x32x16_bf16 v[0:15], v[136:139], v[186:189], v[0:15]
	ds_read_b64_tr_b16 v[186:187], v158 offset:0x2200
	ds_read_b64_tr_b16 v[188:189], v158 offset:0x2a00
	v_mfma_f32_32x32x16_bf16 v[0:15], v[140:143], v[196:199], v[0:15]
	ds_read_b64_tr_b16 v[196:197], v158 offset:0x3200
	ds_read_b64_tr_b16 v[198:199], v158 offset:0x3a00
	s_waitcnt lgkmcnt(0)
	v_mfma_f32_32x32x16_bf16 v[16:31], v[128:131], v[178:181], v[16:31]
	ds_read_b64_tr_b16 v[178:179], v158 offset:0x400
	ds_read_b64_tr_b16 v[180:181], v158 offset:0xc00
	v_mfma_f32_32x32x16_bf16 v[16:31], v[132:135], v[182:185], v[16:31]
	ds_read_b64_tr_b16 v[182:183], v158 offset:0x1400
	ds_read_b64_tr_b16 v[184:185], v158 offset:0x1c00
	v_mfma_f32_32x32x16_bf16 v[16:31], v[136:139], v[186:189], v[16:31]
	ds_read_b64_tr_b16 v[186:187], v158 offset:0x2400
	ds_read_b64_tr_b16 v[188:189], v158 offset:0x2c00
	v_mfma_f32_32x32x16_bf16 v[16:31], v[140:143], v[196:199], v[16:31]
	ds_read_b64_tr_b16 v[196:197], v158 offset:0x3400
	ds_read_b64_tr_b16 v[198:199], v158 offset:0x3c00
	s_waitcnt lgkmcnt(0)
	v_mfma_f32_32x32x16_bf16 v[32:47], v[128:131], v[178:181], v[32:47]
	ds_read_b64_tr_b16 v[178:179], v158 offset:0x600
	ds_read_b64_tr_b16 v[180:181], v158 offset:0xe00
	v_mfma_f32_32x32x16_bf16 v[32:47], v[132:135], v[182:185], v[32:47]
	ds_read_b64_tr_b16 v[182:183], v158 offset:0x1600
	ds_read_b64_tr_b16 v[184:185], v158 offset:0x1e00
	v_mfma_f32_32x32x16_bf16 v[32:47], v[136:139], v[186:189], v[32:47]
	ds_read_b64_tr_b16 v[186:187], v158 offset:0x2600
	ds_read_b64_tr_b16 v[188:189], v158 offset:0x2e00
	v_mfma_f32_32x32x16_bf16 v[32:47], v[140:143], v[196:199], v[32:47]
	ds_read_b64_tr_b16 v[196:197], v158 offset:0x3600
	ds_read_b64_tr_b16 v[198:199], v158 offset:0x3e00
	s_waitcnt lgkmcnt(0)
	v_mfma_f32_32x32x16_bf16 v[48:63], v[128:131], v[178:181], v[48:63]
	s_andn2_b64 vcc, exec, s[22:23]
	v_mfma_f32_32x32x16_bf16 v[48:63], v[132:135], v[182:185], v[48:63]
	v_mfma_f32_32x32x16_bf16 v[48:63], v[136:139], v[186:189], v[48:63]
	v_mfma_f32_32x32x16_bf16 v[48:63], v[140:143], v[196:199], v[48:63]
	s_setprio 0
	s_cbranch_vccnz .LBB0_522
	s_waitcnt vmcnt(0)
	s_waitcnt vmcnt(2)
	ds_write_b128 v211, v[146:149] offset:32768
	s_waitcnt vmcnt(1)
	ds_write_b128 v213, v[150:153]
	s_waitcnt vmcnt(0)
	ds_write_b128 v214, v[154:157]
	s_branch .LBB0_522

.LBB0_548:
	v_lshl_add_u64 v[140:141], v[200:201], 0, s[90:91]
	v_add_co_u32_e32 v64, vcc, s67, v140
	v_lshl_add_u64 v[138:139], v[198:199], 0, s[90:91]
	s_nop 0
	v_addc_co_u32_e32 v65, vcc, 0, v141, vcc
	v_add_co_u32_e32 v66, vcc, s67, v138
	v_lshl_add_u64 v[136:137], v[196:197], 0, s[90:91]
	s_nop 0
	v_addc_co_u32_e32 v67, vcc, 0, v139, vcc
	global_load_dwordx4 v[178:181], v[64:65], off offset:1152
	global_load_dwordx4 v[182:185], v[66:67], off offset:2048
	v_add_co_u32_e32 v64, vcc, s67, v136
	s_nop 1
	v_addc_co_u32_e32 v65, vcc, 0, v137, vcc
	global_load_dwordx4 v[186:189], v[64:65], off offset:2048
	v_add_u32_e32 v142, v206, v207
	v_add_u32_e32 v143, v206, v208
	v_add_u32_e32 v144, v206, v209
	v_add_u32_e32 v145, v206, v210
	ds_read_b128 v[80:83], v142 offset:32768
	ds_read_b128 v[98:101], v142 offset:40960
	ds_read_b128 v[132:135], v143 offset:32768
	ds_read_b128 v[76:79], v143 offset:40960
	ds_read_b128 v[128:131], v144 offset:32768
	ds_read_b128 v[68:71], v144 offset:40960
	ds_read_b128 v[72:75], v145 offset:32768
	ds_read_b128 v[64:67], v145 offset:40960
	s_cmp_eq_u32 s90, 0
	s_cbranch_scc1 .LBB0_550
	ds_read_b64_tr_b16 v[84:85], v217 offset:0
	ds_read_b64_tr_b16 v[86:87], v217 offset:0x800
	ds_read_b64_tr_b16 v[88:89], v217 offset:0x1000
	ds_read_b64_tr_b16 v[90:91], v217 offset:0x1800
	ds_read_b64_tr_b16 v[92:93], v217 offset:0x2000
	ds_read_b64_tr_b16 v[94:95], v217 offset:0x2800
	ds_read_b64_tr_b16 v[102:103], v217 offset:0x3000
	ds_read_b64_tr_b16 v[104:105], v217 offset:0x3800
	s_waitcnt lgkmcnt(0)
	s_nop 0
	s_setprio 1
	v_mfma_f32_32x32x16_bf16 v[0:15], v[112:115], v[84:87], v[0:15]
	ds_read_b64_tr_b16 v[84:85], v217 offset:0x200
	ds_read_b64_tr_b16 v[86:87], v217 offset:0xa00
	v_mfma_f32_32x32x16_bf16 v[0:15], v[116:119], v[88:91], v[0:15]
	ds_read_b64_tr_b16 v[88:89], v217 offset:0x1200
	ds_read_b64_tr_b16 v[90:91], v217 offset:0x1a00
	v_mfma_f32_32x32x16_bf16 v[0:15], v[124:127], v[92:95], v[0:15]
	ds_read_b64_tr_b16 v[92:93], v217 offset:0x2200
	ds_read_b64_tr_b16 v[94:95], v217 offset:0x2a00
	v_mfma_f32_32x32x16_bf16 v[0:15], v[120:123], v[102:105], v[0:15]
	ds_read_b64_tr_b16 v[102:103], v217 offset:0x3200
	ds_read_b64_tr_b16 v[104:105], v217 offset:0x3a00
	s_waitcnt lgkmcnt(0)
	v_mfma_f32_32x32x16_bf16 v[16:31], v[112:115], v[84:87], v[16:31]
	ds_read_b64_tr_b16 v[84:85], v217 offset:0x400
	ds_read_b64_tr_b16 v[86:87], v217 offset:0xc00
	v_mfma_f32_32x32x16_bf16 v[16:31], v[116:119], v[88:91], v[16:31]
	ds_read_b64_tr_b16 v[88:89], v217 offset:0x1400
	ds_read_b64_tr_b16 v[90:91], v217 offset:0x1c00
	v_mfma_f32_32x32x16_bf16 v[16:31], v[124:127], v[92:95], v[16:31]
	ds_read_b64_tr_b16 v[92:93], v217 offset:0x2400
	ds_read_b64_tr_b16 v[94:95], v217 offset:0x2c00
	v_mfma_f32_32x32x16_bf16 v[16:31], v[120:123], v[102:105], v[16:31]
	ds_read_b64_tr_b16 v[102:103], v217 offset:0x3400
	ds_read_b64_tr_b16 v[104:105], v217 offset:0x3c00
	s_waitcnt lgkmcnt(0)
	v_mfma_f32_32x32x16_bf16 v[32:47], v[112:115], v[84:87], v[32:47]
	ds_read_b64_tr_b16 v[84:85], v217 offset:0x600
	ds_read_b64_tr_b16 v[86:87], v217 offset:0xe00
	v_mfma_f32_32x32x16_bf16 v[32:47], v[116:119], v[88:91], v[32:47]
	ds_read_b64_tr_b16 v[88:89], v217 offset:0x1600
	ds_read_b64_tr_b16 v[90:91], v217 offset:0x1e00
	v_mfma_f32_32x32x16_bf16 v[32:47], v[124:127], v[92:95], v[32:47]
	ds_read_b64_tr_b16 v[92:93], v217 offset:0x2600
	ds_read_b64_tr_b16 v[94:95], v217 offset:0x2e00
	v_mfma_f32_32x32x16_bf16 v[32:47], v[120:123], v[102:105], v[32:47]
	ds_read_b64_tr_b16 v[102:103], v217 offset:0x3600
	ds_read_b64_tr_b16 v[104:105], v217 offset:0x3e00
	s_waitcnt lgkmcnt(0)
	v_mfma_f32_32x32x16_bf16 v[48:63], v[112:115], v[84:87], v[48:63]
	v_mfma_f32_32x32x16_bf16 v[48:63], v[116:119], v[88:91], v[48:63]
	v_mfma_f32_32x32x16_bf16 v[48:63], v[124:127], v[92:95], v[48:63]
	v_mfma_f32_32x32x16_bf16 v[48:63], v[120:123], v[102:105], v[48:63]
	s_setprio 0

.LBB0_574:
	v_lshl_add_u64 v[132:133], s[90:91], 0, v[192:193]
	v_add_co_u32_e32 v64, vcc, s67, v132
	v_lshl_add_u64 v[130:131], s[90:91], 0, v[194:195]
	s_nop 0
	v_addc_co_u32_e32 v65, vcc, 0, v133, vcc
	v_add_co_u32_e32 v66, vcc, s67, v130
	v_lshl_add_u64 v[128:129], s[90:91], 0, v[160:161]
	s_nop 0
	v_addc_co_u32_e32 v67, vcc, 0, v131, vcc
	global_load_dwordx4 v[146:149], v[64:65], off offset:1152
	global_load_dwordx4 v[150:153], v[66:67], off offset:2048
	v_add_co_u32_e32 v64, vcc, s67, v128
	s_nop 1
	v_addc_co_u32_e32 v65, vcc, 0, v129, vcc
	global_load_dwordx4 v[154:157], v[64:65], off offset:2048
	v_add_u32_e32 v134, v206, v207
	v_add_u32_e32 v135, v206, v208
	v_add_u32_e32 v136, v206, v209
	v_add_u32_e32 v137, v206, v210
	ds_read_b128 v[64:67], v134 offset:32768
	ds_read_b128 v[68:71], v134 offset:40960
	ds_read_b128 v[72:75], v135 offset:32768
	ds_read_b128 v[76:79], v135 offset:40960
	ds_read_b128 v[80:83], v136 offset:32768
	ds_read_b128 v[84:87], v136 offset:40960
	ds_read_b128 v[88:91], v137 offset:32768
	ds_read_b128 v[92:95], v137 offset:40960
	s_waitcnt lgkmcnt(7)
	s_setprio 1
	v_mfma_f32_32x32x16_bf16 v[112:127], v[64:67], v[162:165], 0
	s_waitcnt lgkmcnt(6)
	v_mfma_f32_32x32x16_bf16 v[96:111], v[68:71], v[162:165], 0
	s_waitcnt lgkmcnt(5)
	v_mfma_f32_32x32x16_bf16 v[112:127], v[72:75], v[166:169], v[112:127]
	s_waitcnt lgkmcnt(4)
	v_mfma_f32_32x32x16_bf16 v[96:111], v[76:79], v[166:169], v[96:111]
	s_waitcnt lgkmcnt(3)
	v_mfma_f32_32x32x16_bf16 v[112:127], v[80:83], v[170:173], v[112:127]
	s_waitcnt lgkmcnt(2)
	v_mfma_f32_32x32x16_bf16 v[96:111], v[84:87], v[170:173], v[96:111]
	s_waitcnt lgkmcnt(1)
	v_mfma_f32_32x32x16_bf16 v[112:127], v[88:91], v[174:177], v[112:127]
	s_waitcnt lgkmcnt(0)
	v_mfma_f32_32x32x16_bf16 v[96:111], v[92:95], v[174:177], v[96:111]
	s_setprio 0
	v_cndmask_b32_e64 v64, 0, 1, s[40:41]
	v_cmp_ne_u32_e64 s[42:43], 1, v64
	s_andn2_b64 vcc, exec, s[40:41]
	s_mov_b64 s[2:3], -1
	s_cbranch_vccnz .LBB0_578
	s_nop 4
	v_exp_f32_e32 v64, v112
	v_exp_f32_e32 v65, v113
	v_exp_f32_e32 v66, v114
	v_exp_f32_e32 v67, v115
	v_exp_f32_e32 v68, v116
	v_exp_f32_e32 v69, v117
	v_exp_f32_e32 v70, v118
	v_exp_f32_e32 v71, v119
	v_exp_f32_e32 v72, v120
	v_exp_f32_e32 v73, v121
	v_exp_f32_e32 v74, v122
	v_exp_f32_e32 v75, v123
	v_exp_f32_e32 v76, v124
	v_exp_f32_e32 v77, v125
	v_exp_f32_e32 v78, v126
	s_cbranch_execz .LBB0_579

.LBB0_582:
	v_exp_f32_e32 v79, v127
	v_exp_f32_e32 v95, v111
	v_cvt_pk_bf16_f32 v96, v64, v65
	v_cvt_pk_bf16_f32 v97, v66, v67
	v_cvt_pk_bf16_f32 v98, v68, v69
	v_cvt_pk_bf16_f32 v99, v70, v71
	v_cvt_pk_bf16_f32 v100, v72, v73
	v_cvt_pk_bf16_f32 v101, v74, v75
	v_cvt_pk_bf16_f32 v102, v76, v77
	v_cvt_pk_bf16_f32 v103, v78, v79
	v_cvt_pk_bf16_f32 v104, v80, v81
	v_cvt_pk_bf16_f32 v105, v82, v83
	v_cvt_pk_bf16_f32 v106, v84, v85
	v_cvt_pk_bf16_f32 v107, v86, v87
	v_cvt_pk_bf16_f32 v108, v88, v89
	v_cvt_pk_bf16_f32 v109, v90, v91
	v_cvt_pk_bf16_f32 v110, v92, v93
	v_cvt_pk_bf16_f32 v111, v94, v95
	v_permlane32_swap_b32_e32 v96, v98
	v_permlane32_swap_b32_e32 v97, v99
	v_permlane32_swap_b32_e32 v100, v102
	v_permlane32_swap_b32_e32 v101, v103
	v_permlane32_swap_b32_e32 v104, v106
	v_permlane32_swap_b32_e32 v105, v107
	v_permlane32_swap_b32_e32 v108, v110
	v_permlane32_swap_b32_e32 v109, v111
	s_barrier
	ds_read_b64_tr_b16 v[112:113], v212 offset:0
	ds_read_b64_tr_b16 v[114:115], v212 offset:0x800
	ds_read_b64_tr_b16 v[116:117], v212 offset:0x1000
	ds_read_b64_tr_b16 v[118:119], v212 offset:0x1800
	ds_read_b64_tr_b16 v[120:121], v212 offset:0x2000
	ds_read_b64_tr_b16 v[122:123], v212 offset:0x2800
	ds_read_b64_tr_b16 v[124:125], v212 offset:0x3000
	ds_read_b64_tr_b16 v[126:127], v212 offset:0x3800
	s_waitcnt lgkmcnt(0)
	s_nop 0
	s_setprio 1
	v_mfma_f32_32x32x16_bf16 v[0:15], v[96:99], v[112:115], v[0:15]
	ds_read_b64_tr_b16 v[112:113], v212 offset:0x200
	ds_read_b64_tr_b16 v[114:115], v212 offset:0xa00
	v_mfma_f32_32x32x16_bf16 v[0:15], v[100:103], v[116:119], v[0:15]
	ds_read_b64_tr_b16 v[116:117], v212 offset:0x1200
	ds_read_b64_tr_b16 v[118:119], v212 offset:0x1a00
	v_mfma_f32_32x32x16_bf16 v[0:15], v[104:107], v[120:123], v[0:15]
	ds_read_b64_tr_b16 v[120:121], v212 offset:0x2200
	ds_read_b64_tr_b16 v[122:123], v212 offset:0x2a00
	v_mfma_f32_32x32x16_bf16 v[0:15], v[108:111], v[124:127], v[0:15]
	ds_read_b64_tr_b16 v[124:125], v212 offset:0x3200
	ds_read_b64_tr_b16 v[126:127], v212 offset:0x3a00
	s_waitcnt lgkmcnt(0)
	v_mfma_f32_32x32x16_bf16 v[16:31], v[96:99], v[112:115], v[16:31]
	ds_read_b64_tr_b16 v[112:113], v212 offset:0x400
	ds_read_b64_tr_b16 v[114:115], v212 offset:0xc00
	v_mfma_f32_32x32x16_bf16 v[16:31], v[100:103], v[116:119], v[16:31]
	ds_read_b64_tr_b16 v[116:117], v212 offset:0x1400
	ds_read_b64_tr_b16 v[118:119], v212 offset:0x1c00
	v_mfma_f32_32x32x16_bf16 v[16:31], v[104:107], v[120:123], v[16:31]
	ds_read_b64_tr_b16 v[120:121], v212 offset:0x2400
	ds_read_b64_tr_b16 v[122:123], v212 offset:0x2c00
	v_mfma_f32_32x32x16_bf16 v[16:31], v[108:111], v[124:127], v[16:31]
	ds_read_b64_tr_b16 v[124:125], v212 offset:0x3400
	ds_read_b64_tr_b16 v[126:127], v212 offset:0x3c00
	s_waitcnt lgkmcnt(0)
	v_mfma_f32_32x32x16_bf16 v[32:47], v[96:99], v[112:115], v[32:47]
	ds_read_b64_tr_b16 v[112:113], v212 offset:0x600
	ds_read_b64_tr_b16 v[114:115], v212 offset:0xe00
	v_mfma_f32_32x32x16_bf16 v[32:47], v[100:103], v[116:119], v[32:47]
	ds_read_b64_tr_b16 v[116:117], v212 offset:0x1600
	ds_read_b64_tr_b16 v[118:119], v212 offset:0x1e00
	v_mfma_f32_32x32x16_bf16 v[32:47], v[104:107], v[120:123], v[32:47]
	ds_read_b64_tr_b16 v[120:121], v212 offset:0x2600
	ds_read_b64_tr_b16 v[122:123], v212 offset:0x2e00
	v_mfma_f32_32x32x16_bf16 v[32:47], v[108:111], v[124:127], v[32:47]
	ds_read_b64_tr_b16 v[124:125], v212 offset:0x3600
	ds_read_b64_tr_b16 v[126:127], v212 offset:0x3e00
	s_waitcnt lgkmcnt(0)
	v_mfma_f32_32x32x16_bf16 v[48:63], v[96:99], v[112:115], v[48:63]
	s_setprio 0
	s_cmp_lt_u32 s6, 30
	s_waitcnt vmcnt(0)
	s_cselect_b64 s[22:23], -1, 0
	s_cmp_gt_u32 s6, 29
	s_cselect_b64 s[2:3], -1, 0
	s_and_b64 vcc, exec, s[2:3]
	s_waitcnt vmcnt(2)
	ds_write_b128 v211, v[146:149] offset:49152
	s_waitcnt vmcnt(1)
	ds_write_b128 v213, v[150:153] offset:16384
	s_waitcnt vmcnt(0)
	ds_write_b128 v214, v[154:157] offset:16384
	v_mfma_f32_32x32x16_bf16 v[48:63], v[100:103], v[116:119], v[48:63]
	s_waitcnt lgkmcnt(0)
	s_barrier
	v_mfma_f32_32x32x16_bf16 v[48:63], v[104:107], v[120:123], v[48:63]
	v_mfma_f32_32x32x16_bf16 v[48:63], v[108:111], v[124:127], v[48:63]
	s_cbranch_vccnz .LBB0_584
	v_add_co_u32_e32 v96, vcc, 0x64d0000, v132
	s_nop 1
	v_addc_co_u32_e32 v97, vcc, 0, v133, vcc
	v_add_co_u32_e32 v98, vcc, 0x64d0000, v130
	s_nop 1
	v_addc_co_u32_e32 v99, vcc, 0, v131, vcc
	global_load_dwordx4 v[146:149], v[96:97], off offset:1152
	global_load_dwordx4 v[150:153], v[98:99], off offset:2048
	v_add_co_u32_e32 v96, vcc, 0x64d0000, v128
	s_nop 1
	v_addc_co_u32_e32 v97, vcc, 0, v129, vcc
	global_load_dwordx4 v[154:157], v[96:97], off offset:2048

.LBB0_601:
	v_pk_add_f32 v[64:65], v[96:97], 0 op_sel_hi:[1,0]
	v_exp_f32_e32 v143, v95
	v_pk_add_f32 v[64:65], v[64:65], v[112:113]
	v_exp_f32_e32 v159, v79
	v_pk_add_f32 v[64:65], v[98:99], v[64:65]
	v_cvt_pk_bf16_f32 v66, v132, v133
	v_pk_add_f32 v[64:65], v[114:115], v[64:65]
	v_cvt_pk_bf16_f32 v67, v134, v135
	v_pk_add_f32 v[64:65], v[100:101], v[64:65]
	v_cvt_pk_bf16_f32 v68, v136, v137
	v_pk_add_f32 v[64:65], v[116:117], v[64:65]
	v_cvt_pk_bf16_f32 v69, v138, v139
	v_pk_add_f32 v[64:65], v[102:103], v[64:65]
	v_cvt_pk_bf16_f32 v70, v140, v141
	v_pk_add_f32 v[64:65], v[118:119], v[64:65]
	v_cvt_pk_bf16_f32 v71, v142, v143
	v_pk_add_f32 v[64:65], v[104:105], v[64:65]
	v_cvt_pk_bf16_f32 v72, v144, v145
	v_pk_add_f32 v[64:65], v[120:121], v[64:65]
	v_cvt_pk_bf16_f32 v73, v146, v147
	v_pk_add_f32 v[64:65], v[106:107], v[64:65]
	v_cvt_pk_bf16_f32 v74, v148, v149
	v_pk_add_f32 v[64:65], v[122:123], v[64:65]
	v_cvt_pk_bf16_f32 v75, v150, v151
	v_pk_add_f32 v[64:65], v[108:109], v[64:65]
	v_cvt_pk_bf16_f32 v76, v152, v153
	v_pk_add_f32 v[64:65], v[124:125], v[64:65]
	v_cvt_pk_bf16_f32 v77, v154, v155
	v_pk_add_f32 v[64:65], v[110:111], v[64:65]
	v_cvt_pk_bf16_f32 v78, v156, v157
	v_pk_add_f32 v[64:65], v[126:127], v[64:65]
	v_cvt_pk_bf16_f32 v79, v158, v159
	v_add_f32_e32 v64, v64, v65
	v_add_f32_e32 v229, v229, v64
	v_pk_add_f32 v[64:65], v[128:129], 0 op_sel_hi:[1,0]
	v_permlane32_swap_b32_e32 v68, v70
	v_pk_add_f32 v[64:65], v[64:65], v[144:145]
	v_permlane32_swap_b32_e32 v69, v71
	v_pk_add_f32 v[64:65], v[130:131], v[64:65]
	v_permlane32_swap_b32_e32 v72, v74
	v_pk_add_f32 v[64:65], v[146:147], v[64:65]
	v_permlane32_swap_b32_e32 v73, v75
	v_pk_add_f32 v[64:65], v[132:133], v[64:65]
	v_permlane32_swap_b32_e32 v76, v78
	v_pk_add_f32 v[64:65], v[148:149], v[64:65]
	v_permlane32_swap_b32_e32 v77, v79
	v_pk_add_f32 v[64:65], v[134:135], v[64:65]
	s_nop 0
	v_pk_add_f32 v[64:65], v[150:151], v[64:65]
	s_nop 0
	v_pk_add_f32 v[64:65], v[136:137], v[64:65]
	s_nop 0
	v_pk_add_f32 v[64:65], v[152:153], v[64:65]
	s_nop 0
	v_pk_add_f32 v[64:65], v[138:139], v[64:65]
	s_nop 0
	v_pk_add_f32 v[64:65], v[154:155], v[64:65]
	s_nop 0
	v_pk_add_f32 v[64:65], v[140:141], v[64:65]
	s_nop 0
	v_pk_add_f32 v[64:65], v[156:157], v[64:65]
	s_nop 0
	v_pk_add_f32 v[64:65], v[142:143], v[64:65]
	s_nop 0
	v_pk_add_f32 v[64:65], v[158:159], v[64:65]
	s_nop 0
	v_add_f32_e32 v64, v64, v65
	v_add_f32_e32 v160, v160, v64
	v_cvt_pk_bf16_f32 v64, v128, v129
	v_cvt_pk_bf16_f32 v65, v130, v131
	s_nop 0
	v_permlane32_swap_b32_e32 v64, v66
	v_permlane32_swap_b32_e32 v65, v67
	v_lshl_add_u32 v96, s23, 13, v228
	ds_read_b64_tr_b16 v[80:81], v96 offset:0
	ds_read_b64_tr_b16 v[82:83], v96 offset:0x400
	ds_read_b64_tr_b16 v[84:85], v96 offset:0x800
	ds_read_b64_tr_b16 v[86:87], v96 offset:0xc00
	ds_read_b64_tr_b16 v[88:89], v96 offset:0x1000
	ds_read_b64_tr_b16 v[90:91], v96 offset:0x1400
	ds_read_b64_tr_b16 v[92:93], v96 offset:0x1800
	ds_read_b64_tr_b16 v[94:95], v96 offset:0x1c00
	s_waitcnt lgkmcnt(0)
	s_nop 0
	s_setprio 1
	v_mfma_f32_32x32x16_bf16 v[48:63], v[210:213], v[80:83], v[48:63]
	v_mfma_f32_32x32x16_bf16 v[0:15], v[64:67], v[80:83], v[0:15]
	ds_read_b64_tr_b16 v[80:81], v96 offset:0x200
	ds_read_b64_tr_b16 v[82:83], v96 offset:0x600
	v_mfma_f32_32x32x16_bf16 v[48:63], v[218:221], v[84:87], v[48:63]
	v_mfma_f32_32x32x16_bf16 v[0:15], v[68:71], v[84:87], v[0:15]
	ds_read_b64_tr_b16 v[84:85], v96 offset:0xa00
	ds_read_b64_tr_b16 v[86:87], v96 offset:0xe00
	v_mfma_f32_32x32x16_bf16 v[48:63], v[222:225], v[88:91], v[48:63]
	v_mfma_f32_32x32x16_bf16 v[0:15], v[72:75], v[88:91], v[0:15]
	ds_read_b64_tr_b16 v[88:89], v96 offset:0x1200
	ds_read_b64_tr_b16 v[90:91], v96 offset:0x1600
	v_mfma_f32_32x32x16_bf16 v[48:63], v[214:217], v[92:95], v[48:63]
	v_mfma_f32_32x32x16_bf16 v[0:15], v[76:79], v[92:95], v[0:15]
	ds_read_b64_tr_b16 v[92:93], v96 offset:0x1a00
	ds_read_b64_tr_b16 v[94:95], v96 offset:0x1e00
	s_waitcnt lgkmcnt(0)
	v_mfma_f32_32x32x16_bf16 v[32:47], v[210:213], v[80:83], v[32:47]
	s_waitcnt vmcnt(0)
	s_add_u32 s74, s74, 0x18000
	s_addc_u32 s75, s75, 0
	s_add_i32 s22, s22, 1
	v_lshl_add_u64 v[236:237], v[236:237], 0, s[20:21]
	s_cmp_eq_u32 s74, 0x300000
	s_waitcnt vmcnt(0)
	v_mfma_f32_32x32x16_bf16 v[16:31], v[64:67], v[80:83], v[16:31]
	s_setprio 0
	s_barrier
	s_setprio 1
	v_mfma_f32_32x32x16_bf16 v[32:47], v[218:221], v[84:87], v[32:47]
	v_mfma_f32_32x32x16_bf16 v[16:31], v[68:71], v[84:87], v[16:31]
	v_mfma_f32_32x32x16_bf16 v[32:47], v[222:225], v[88:91], v[32:47]
	v_mfma_f32_32x32x16_bf16 v[16:31], v[72:75], v[88:91], v[16:31]
	v_mfma_f32_32x32x16_bf16 v[32:47], v[214:217], v[92:95], v[32:47]
	v_mfma_f32_32x32x16_bf16 v[16:31], v[76:79], v[92:95], v[16:31]
	s_setprio 0
	s_cbranch_scc1 .LBB0_622

.LBB0_606:
	v_lshl_add_u32 v64, v246, 8, 0
	v_add_u32_e32 v112, s44, v64
	v_add_u32_e32 v68, v112, v226
	v_add_u32_e32 v72, v112, v227
	ds_read_b128 v[64:67], v68 offset:32768
	ds_read_b128 v[68:71], v68 offset:40960
	ds_read_b128 v[96:99], v72 offset:32768
	ds_read_b128 v[100:103], v72 offset:40960
	s_waitcnt lgkmcnt(0)
	s_setprio 1
	v_mfma_f32_32x32x16_bf16 v[114:129], v[64:67], v[162:165], 0
	v_mfma_f32_32x32x16_bf16 v[80:95], v[64:67], v[186:189], 0
	v_mfma_f32_32x32x16_bf16 v[130:145], v[68:71], v[162:165], 0
	v_mfma_f32_32x32x16_bf16 v[64:79], v[68:71], v[186:189], 0
	v_mfma_f32_32x32x16_bf16 v[114:129], v[96:99], v[166:169], v[114:129]
	v_mfma_f32_32x32x16_bf16 v[80:95], v[96:99], v[190:193], v[80:95]
	v_mfma_f32_32x32x16_bf16 v[130:145], v[100:103], v[166:169], v[130:145]
	v_mfma_f32_32x32x16_bf16 v[64:79], v[100:103], v[190:193], v[64:79]
	v_add_u32_e32 v100, v112, v238
	v_add_u32_e32 v108, v112, v239
	ds_read_b128 v[96:99], v100 offset:32768
	ds_read_b128 v[100:103], v100 offset:40960
	ds_read_b128 v[104:107], v108 offset:32768
	ds_read_b128 v[108:111], v108 offset:40960
	s_waitcnt lgkmcnt(0)
	v_mfma_f32_32x32x16_bf16 v[114:129], v[96:99], v[170:173], v[114:129]
	v_mfma_f32_32x32x16_bf16 v[80:95], v[96:99], v[194:197], v[80:95]
	v_mfma_f32_32x32x16_bf16 v[130:145], v[100:103], v[170:173], v[130:145]
	v_mfma_f32_32x32x16_bf16 v[64:79], v[100:103], v[194:197], v[64:79]
	v_mfma_f32_32x32x16_bf16 v[114:129], v[104:107], v[174:177], v[114:129]
	v_mfma_f32_32x32x16_bf16 v[80:95], v[104:107], v[198:201], v[80:95]
	v_mfma_f32_32x32x16_bf16 v[130:145], v[108:111], v[174:177], v[130:145]
	v_mfma_f32_32x32x16_bf16 v[64:79], v[108:111], v[198:201], v[64:79]
	v_add_u32_e32 v100, v112, v247
	v_add_u32_e32 v108, v112, v249
	ds_read_b128 v[96:99], v100 offset:32768
	ds_read_b128 v[100:103], v100 offset:40960
	ds_read_b128 v[104:107], v108 offset:32768
	ds_read_b128 v[108:111], v108 offset:40960
	s_waitcnt lgkmcnt(0)
	v_mfma_f32_32x32x16_bf16 v[114:129], v[96:99], v[178:181], v[114:129]
	v_mfma_f32_32x32x16_bf16 v[80:95], v[96:99], v[202:205], v[80:95]
	v_mfma_f32_32x32x16_bf16 v[130:145], v[100:103], v[178:181], v[130:145]
	v_mfma_f32_32x32x16_bf16 v[64:79], v[100:103], v[202:205], v[64:79]
	v_mfma_f32_32x32x16_bf16 v[114:129], v[104:107], v[182:185], v[114:129]
	v_mfma_f32_32x32x16_bf16 v[80:95], v[104:107], v[206:209], v[80:95]
	v_mfma_f32_32x32x16_bf16 v[130:145], v[108:111], v[182:185], v[130:145]
	v_mfma_f32_32x32x16_bf16 v[64:79], v[108:111], v[206:209], v[64:79]
	s_setprio 0
	v_cndmask_b32_e64 v96, 0, 1, s[40:41]
	v_cmp_ne_u32_e64 s[44:45], 1, v96
	s_andn2_b64 vcc, exec, s[40:41]
	s_mov_b64 s[2:3], -1
	s_cbranch_vccnz .LBB0_610
	s_nop 3
	v_exp_f32_e32 v96, v114
	v_exp_f32_e32 v97, v115
	v_exp_f32_e32 v98, v116
	v_exp_f32_e32 v99, v117
	v_exp_f32_e32 v100, v118
	v_exp_f32_e32 v101, v119
	v_exp_f32_e32 v102, v120
	v_exp_f32_e32 v103, v121
	v_exp_f32_e32 v104, v122
	v_exp_f32_e32 v105, v123
	v_exp_f32_e32 v106, v124
	v_exp_f32_e32 v107, v125
	v_exp_f32_e32 v108, v126
	v_exp_f32_e32 v109, v127
	v_exp_f32_e32 v110, v128
	s_cbranch_execz .LBB0_611

.LBB0_631:
	v_pk_add_f32 v[64:65], v[96:97], 0 op_sel_hi:[1,0]
	v_exp_f32_e32 v143, v95
	v_pk_add_f32 v[64:65], v[64:65], v[112:113]
	v_exp_f32_e32 v159, v79
	v_pk_add_f32 v[64:65], v[98:99], v[64:65]
	v_cvt_pk_bf16_f32 v66, v132, v133
	v_pk_add_f32 v[64:65], v[114:115], v[64:65]
	v_cvt_pk_bf16_f32 v67, v134, v135
	v_pk_add_f32 v[64:65], v[100:101], v[64:65]
	v_cvt_pk_bf16_f32 v68, v136, v137
	v_pk_add_f32 v[64:65], v[116:117], v[64:65]
	v_cvt_pk_bf16_f32 v69, v138, v139
	v_pk_add_f32 v[64:65], v[102:103], v[64:65]
	v_cvt_pk_bf16_f32 v70, v140, v141
	v_pk_add_f32 v[64:65], v[118:119], v[64:65]
	v_cvt_pk_bf16_f32 v71, v142, v143
	v_pk_add_f32 v[64:65], v[104:105], v[64:65]
	v_cvt_pk_bf16_f32 v72, v144, v145
	v_pk_add_f32 v[64:65], v[120:121], v[64:65]
	v_cvt_pk_bf16_f32 v73, v146, v147
	v_pk_add_f32 v[64:65], v[106:107], v[64:65]
	v_cvt_pk_bf16_f32 v74, v148, v149
	v_pk_add_f32 v[64:65], v[122:123], v[64:65]
	v_cvt_pk_bf16_f32 v75, v150, v151
	v_pk_add_f32 v[64:65], v[108:109], v[64:65]
	v_cvt_pk_bf16_f32 v76, v152, v153
	v_pk_add_f32 v[64:65], v[124:125], v[64:65]
	v_cvt_pk_bf16_f32 v77, v154, v155
	v_pk_add_f32 v[64:65], v[110:111], v[64:65]
	v_cvt_pk_bf16_f32 v78, v156, v157
	v_pk_add_f32 v[64:65], v[126:127], v[64:65]
	v_cvt_pk_bf16_f32 v79, v158, v159
	v_add_f32_e32 v64, v64, v65
	v_add_f32_e32 v227, v227, v64
	v_pk_add_f32 v[64:65], v[128:129], 0 op_sel_hi:[1,0]
	v_permlane32_swap_b32_e32 v68, v70
	v_pk_add_f32 v[64:65], v[64:65], v[144:145]
	v_permlane32_swap_b32_e32 v69, v71
	v_pk_add_f32 v[64:65], v[130:131], v[64:65]
	v_permlane32_swap_b32_e32 v72, v74
	v_pk_add_f32 v[64:65], v[146:147], v[64:65]
	v_permlane32_swap_b32_e32 v73, v75
	v_pk_add_f32 v[64:65], v[132:133], v[64:65]
	v_permlane32_swap_b32_e32 v76, v78
	v_pk_add_f32 v[64:65], v[148:149], v[64:65]
	v_permlane32_swap_b32_e32 v77, v79
	v_pk_add_f32 v[64:65], v[134:135], v[64:65]
	s_nop 0
	v_pk_add_f32 v[64:65], v[150:151], v[64:65]
	s_nop 0
	v_pk_add_f32 v[64:65], v[136:137], v[64:65]
	s_nop 0
	v_pk_add_f32 v[64:65], v[152:153], v[64:65]
	s_nop 0
	v_pk_add_f32 v[64:65], v[138:139], v[64:65]
	s_nop 0
	v_pk_add_f32 v[64:65], v[154:155], v[64:65]
	s_nop 0
	v_pk_add_f32 v[64:65], v[140:141], v[64:65]
	s_nop 0
	v_pk_add_f32 v[64:65], v[156:157], v[64:65]
	s_nop 0
	v_pk_add_f32 v[64:65], v[142:143], v[64:65]
	s_nop 0
	v_pk_add_f32 v[64:65], v[158:159], v[64:65]
	s_nop 0
	v_add_f32_e32 v64, v64, v65
	v_add_f32_e32 v160, v160, v64
	v_cvt_pk_bf16_f32 v64, v128, v129
	v_cvt_pk_bf16_f32 v65, v130, v131
	s_nop 0
	v_permlane32_swap_b32_e32 v64, v66
	v_permlane32_swap_b32_e32 v65, v67
	v_lshl_add_u32 v96, s33, 13, v226
	ds_read_b64_tr_b16 v[80:81], v96 offset:0
	ds_read_b64_tr_b16 v[82:83], v96 offset:0x400
	ds_read_b64_tr_b16 v[84:85], v96 offset:0x800
	ds_read_b64_tr_b16 v[86:87], v96 offset:0xc00
	ds_read_b64_tr_b16 v[88:89], v96 offset:0x1000
	ds_read_b64_tr_b16 v[90:91], v96 offset:0x1400
	ds_read_b64_tr_b16 v[92:93], v96 offset:0x1800
	ds_read_b64_tr_b16 v[94:95], v96 offset:0x1c00
	s_waitcnt lgkmcnt(0)
	s_nop 0
	s_setprio 1
	v_mfma_f32_32x32x16_bf16 v[48:63], v[194:197], v[80:83], v[48:63]
	v_mfma_f32_32x32x16_bf16 v[0:15], v[64:67], v[80:83], v[0:15]
	ds_read_b64_tr_b16 v[80:81], v96 offset:0x200
	ds_read_b64_tr_b16 v[82:83], v96 offset:0x600
	v_mfma_f32_32x32x16_bf16 v[48:63], v[198:201], v[84:87], v[48:63]
	v_mfma_f32_32x32x16_bf16 v[0:15], v[68:71], v[84:87], v[0:15]
	ds_read_b64_tr_b16 v[84:85], v96 offset:0xa00
	ds_read_b64_tr_b16 v[86:87], v96 offset:0xe00
	v_mfma_f32_32x32x16_bf16 v[48:63], v[202:205], v[88:91], v[48:63]
	v_mfma_f32_32x32x16_bf16 v[0:15], v[72:75], v[88:91], v[0:15]
	ds_read_b64_tr_b16 v[88:89], v96 offset:0x1200
	ds_read_b64_tr_b16 v[90:91], v96 offset:0x1600
	v_mfma_f32_32x32x16_bf16 v[48:63], v[206:209], v[92:95], v[48:63]
	v_mfma_f32_32x32x16_bf16 v[0:15], v[76:79], v[92:95], v[0:15]
	ds_read_b64_tr_b16 v[92:93], v96 offset:0x1a00
	ds_read_b64_tr_b16 v[94:95], v96 offset:0x1e00
	s_waitcnt lgkmcnt(0)
	v_mfma_f32_32x32x16_bf16 v[32:47], v[194:197], v[80:83], v[32:47]
	s_setprio 0
	s_waitcnt vmcnt(0)
	s_add_u32 s90, s90, 0x68000
	s_addc_u32 s91, s91, 0
	s_add_i32 s31, s31, 1
	s_cmp_eq_u32 s90, 0xd00000
	s_waitcnt vmcnt(0)
	s_barrier
	s_setprio 1
	v_mfma_f32_32x32x16_bf16 v[16:31], v[64:67], v[80:83], v[16:31]
	v_mfma_f32_32x32x16_bf16 v[32:47], v[198:201], v[84:87], v[32:47]
	v_mfma_f32_32x32x16_bf16 v[16:31], v[68:71], v[84:87], v[16:31]
	v_mfma_f32_32x32x16_bf16 v[32:47], v[202:205], v[88:91], v[32:47]
	v_mfma_f32_32x32x16_bf16 v[16:31], v[72:75], v[88:91], v[16:31]
	v_mfma_f32_32x32x16_bf16 v[32:47], v[206:209], v[92:95], v[32:47]
	v_mfma_f32_32x32x16_bf16 v[16:31], v[76:79], v[92:95], v[16:31]
	s_setprio 0
	s_cbranch_scc1 .LBB0_652

.LBB0_636:
	v_add_u32_e32 v104, s44, v221
	v_add_u32_e32 v68, v104, v222
	v_add_u32_e32 v72, v104, v223
	ds_read_b128 v[64:67], v68 offset:32768
	ds_read_b128 v[68:71], v68 offset:40960
	ds_read_b128 v[96:99], v72 offset:32768
	ds_read_b128 v[100:103], v72 offset:40960
	s_waitcnt lgkmcnt(0)
	s_setprio 1
	v_mfma_f32_32x32x16_bf16 v[114:129], v[64:67], v[162:165], 0
	v_mfma_f32_32x32x16_bf16 v[80:95], v[64:67], v[178:181], 0
	v_mfma_f32_32x32x16_bf16 v[130:145], v[68:71], v[162:165], 0
	v_mfma_f32_32x32x16_bf16 v[64:79], v[68:71], v[178:181], 0
	v_mfma_f32_32x32x16_bf16 v[114:129], v[96:99], v[166:169], v[114:129]
	v_mfma_f32_32x32x16_bf16 v[80:95], v[96:99], v[182:185], v[80:95]
	v_mfma_f32_32x32x16_bf16 v[130:145], v[100:103], v[166:169], v[130:145]
	v_mfma_f32_32x32x16_bf16 v[64:79], v[100:103], v[182:185], v[64:79]
	v_add_u32_e32 v100, v104, v224
	v_add_u32_e32 v108, v104, v225
	ds_read_b128 v[96:99], v100 offset:32768
	ds_read_b128 v[100:103], v100 offset:40960
	ds_read_b128 v[104:107], v108 offset:32768
	ds_read_b128 v[108:111], v108 offset:40960
	s_waitcnt lgkmcnt(0)
	v_mfma_f32_32x32x16_bf16 v[114:129], v[96:99], v[170:173], v[114:129]
	v_mfma_f32_32x32x16_bf16 v[80:95], v[96:99], v[186:189], v[80:95]
	v_mfma_f32_32x32x16_bf16 v[130:145], v[100:103], v[170:173], v[130:145]
	v_mfma_f32_32x32x16_bf16 v[64:79], v[100:103], v[186:189], v[64:79]
	v_mfma_f32_32x32x16_bf16 v[114:129], v[104:107], v[174:177], v[114:129]
	v_mfma_f32_32x32x16_bf16 v[80:95], v[104:107], v[190:193], v[80:95]
	v_mfma_f32_32x32x16_bf16 v[130:145], v[108:111], v[174:177], v[130:145]
	v_mfma_f32_32x32x16_bf16 v[64:79], v[108:111], v[190:193], v[64:79]
	s_setprio 0
	v_cndmask_b32_e64 v96, 0, 1, s[40:41]
	v_cmp_ne_u32_e64 s[44:45], 1, v96
	s_andn2_b64 vcc, exec, s[40:41]
	s_mov_b64 s[2:3], -1
	s_cbranch_vccnz .LBB0_640
	s_nop 3
	v_exp_f32_e32 v96, v114
	v_exp_f32_e32 v97, v115
	v_exp_f32_e32 v98, v116
	v_exp_f32_e32 v99, v117
	v_exp_f32_e32 v100, v118
	v_exp_f32_e32 v101, v119
	v_exp_f32_e32 v102, v120
	v_exp_f32_e32 v103, v121
	v_exp_f32_e32 v104, v122
	v_exp_f32_e32 v105, v123
	v_exp_f32_e32 v106, v124
	v_exp_f32_e32 v107, v125
	v_exp_f32_e32 v108, v126
	v_exp_f32_e32 v109, v127
	v_exp_f32_e32 v110, v128
	s_cbranch_execz .LBB0_641

.LBB0_661:
	s_lshl_b64 s[2:3], s[2:3], 1
	s_add_u32 s2, s18, s2
	s_addc_u32 s3, s19, s3
	global_load_dwordx4 v[194:197], v210, s[2:3]
	global_load_dwordx4 v[198:201], v210, s[2:3] offset:256
	global_load_dwordx4 v[202:205], v212, s[2:3]
	global_load_dwordx4 v[206:209], v212, s[2:3] offset:256
	s_and_b64 vcc, exec, s[48:49]
	s_cbranch_vccnz .LBB0_663
	ds_read_b64_tr_b16 v[64:65], v239 offset:0
	ds_read_b64_tr_b16 v[66:67], v239 offset:0x800
	ds_read_b64_tr_b16 v[68:69], v239 offset:0x1000
	ds_read_b64_tr_b16 v[70:71], v239 offset:0x1800
	ds_read_b64_tr_b16 v[72:73], v239 offset:0x2000
	ds_read_b64_tr_b16 v[74:75], v239 offset:0x2800
	ds_read_b64_tr_b16 v[76:77], v239 offset:0x3000
	ds_read_b64_tr_b16 v[78:79], v239 offset:0x3800
	s_waitcnt lgkmcnt(0)
	s_nop 0
	s_setprio 1
	v_mfma_f32_32x32x16_bf16 v[0:15], v[124:127], v[64:67], v[0:15]
	ds_read_b64_tr_b16 v[64:65], v239 offset:0x200
	ds_read_b64_tr_b16 v[66:67], v239 offset:0xa00
	v_mfma_f32_32x32x16_bf16 v[0:15], v[120:123], v[68:71], v[0:15]
	ds_read_b64_tr_b16 v[68:69], v239 offset:0x1200
	ds_read_b64_tr_b16 v[70:71], v239 offset:0x1a00
	v_mfma_f32_32x32x16_bf16 v[0:15], v[116:119], v[72:75], v[0:15]
	ds_read_b64_tr_b16 v[72:73], v239 offset:0x2200
	ds_read_b64_tr_b16 v[74:75], v239 offset:0x2a00
	v_mfma_f32_32x32x16_bf16 v[0:15], v[112:115], v[76:79], v[0:15]
	ds_read_b64_tr_b16 v[76:77], v239 offset:0x3200
	ds_read_b64_tr_b16 v[78:79], v239 offset:0x3a00
	s_waitcnt lgkmcnt(0)
	v_mfma_f32_32x32x16_bf16 v[16:31], v[124:127], v[64:67], v[16:31]
	ds_read_b64_tr_b16 v[64:65], v239 offset:0x400
	ds_read_b64_tr_b16 v[66:67], v239 offset:0xc00
	v_mfma_f32_32x32x16_bf16 v[16:31], v[120:123], v[68:71], v[16:31]
	ds_read_b64_tr_b16 v[68:69], v239 offset:0x1400
	ds_read_b64_tr_b16 v[70:71], v239 offset:0x1c00
	v_mfma_f32_32x32x16_bf16 v[16:31], v[116:119], v[72:75], v[16:31]
	ds_read_b64_tr_b16 v[72:73], v239 offset:0x2400
	ds_read_b64_tr_b16 v[74:75], v239 offset:0x2c00
	v_mfma_f32_32x32x16_bf16 v[16:31], v[112:115], v[76:79], v[16:31]
	ds_read_b64_tr_b16 v[76:77], v239 offset:0x3400
	ds_read_b64_tr_b16 v[78:79], v239 offset:0x3c00
	s_waitcnt lgkmcnt(0)
	v_mfma_f32_32x32x16_bf16 v[32:47], v[124:127], v[64:67], v[32:47]
	ds_read_b64_tr_b16 v[64:65], v239 offset:0x600
	ds_read_b64_tr_b16 v[66:67], v239 offset:0xe00
	v_mfma_f32_32x32x16_bf16 v[32:47], v[120:123], v[68:71], v[32:47]
	ds_read_b64_tr_b16 v[68:69], v239 offset:0x1600
	ds_read_b64_tr_b16 v[70:71], v239 offset:0x1e00
	v_mfma_f32_32x32x16_bf16 v[32:47], v[116:119], v[72:75], v[32:47]
	ds_read_b64_tr_b16 v[72:73], v239 offset:0x2600
	ds_read_b64_tr_b16 v[74:75], v239 offset:0x2e00
	v_mfma_f32_32x32x16_bf16 v[32:47], v[112:115], v[76:79], v[32:47]
	ds_read_b64_tr_b16 v[76:77], v239 offset:0x3600
	ds_read_b64_tr_b16 v[78:79], v239 offset:0x3e00
	s_waitcnt lgkmcnt(0)
	v_mfma_f32_32x32x16_bf16 v[48:63], v[124:127], v[64:67], v[48:63]
	v_mfma_f32_32x32x16_bf16 v[48:63], v[120:123], v[68:71], v[48:63]
	v_mfma_f32_32x32x16_bf16 v[48:63], v[116:119], v[72:75], v[48:63]
	v_mfma_f32_32x32x16_bf16 v[48:63], v[112:115], v[76:79], v[48:63]
	s_setprio 0
.LBB0_663:
	ds_read_b128 v[64:67], v213 offset:32768
	ds_read_b128 v[68:71], v213 offset:40960
	ds_read_b128 v[72:75], v241 offset:32768
	ds_read_b128 v[76:79], v241 offset:40960
	ds_read_b128 v[114:117], v244 offset:32768
	ds_read_b128 v[118:121], v244 offset:40960
	ds_read_b128 v[122:125], v246 offset:32768
	ds_read_b128 v[126:129], v246 offset:40960
	s_waitcnt lgkmcnt(7)
	s_setprio 1
	v_mfma_f32_32x32x16_bf16 v[82:97], v[64:67], v[162:165], 0
	s_waitcnt lgkmcnt(6)
	v_mfma_f32_32x32x16_bf16 v[98:113], v[68:71], v[162:165], 0
	s_waitcnt lgkmcnt(5)
	v_mfma_f32_32x32x16_bf16 v[82:97], v[72:75], v[166:169], v[82:97]
	s_waitcnt lgkmcnt(4)
	v_mfma_f32_32x32x16_bf16 v[98:113], v[76:79], v[166:169], v[98:113]
	s_waitcnt lgkmcnt(3)
	v_mfma_f32_32x32x16_bf16 v[82:97], v[114:117], v[170:173], v[82:97]
	s_waitcnt lgkmcnt(2)
	v_mfma_f32_32x32x16_bf16 v[98:113], v[118:121], v[170:173], v[98:113]
	s_waitcnt lgkmcnt(1)
	v_mfma_f32_32x32x16_bf16 v[82:97], v[122:125], v[174:177], v[82:97]
	s_waitcnt lgkmcnt(0)
	v_mfma_f32_32x32x16_bf16 v[98:113], v[126:129], v[174:177], v[98:113]
	ds_read_b128 v[64:67], v247 offset:32768
	ds_read_b128 v[68:71], v247 offset:40960
	ds_read_b128 v[72:75], v249 offset:32768
	ds_read_b128 v[76:79], v249 offset:40960
	ds_read_b128 v[114:117], v226 offset:32768
	ds_read_b128 v[118:121], v226 offset:40960
	ds_read_b128 v[122:125], v227 offset:32768
	ds_read_b128 v[126:129], v227 offset:40960
	s_waitcnt lgkmcnt(7)
	v_mfma_f32_32x32x16_bf16 v[82:97], v[64:67], v[178:181], v[82:97]
	s_waitcnt lgkmcnt(6)
	v_mfma_f32_32x32x16_bf16 v[98:113], v[68:71], v[178:181], v[98:113]
	s_waitcnt lgkmcnt(5)
	v_mfma_f32_32x32x16_bf16 v[82:97], v[72:75], v[182:185], v[82:97]
	s_waitcnt lgkmcnt(4)
	v_mfma_f32_32x32x16_bf16 v[98:113], v[76:79], v[182:185], v[98:113]
	s_waitcnt lgkmcnt(3)
	v_mfma_f32_32x32x16_bf16 v[82:97], v[114:117], v[186:189], v[82:97]
	s_waitcnt lgkmcnt(2)
	v_mfma_f32_32x32x16_bf16 v[98:113], v[118:121], v[186:189], v[98:113]
	s_waitcnt lgkmcnt(1)
	v_mfma_f32_32x32x16_bf16 v[82:97], v[122:125], v[190:193], v[82:97]
	s_waitcnt lgkmcnt(0)
	v_mfma_f32_32x32x16_bf16 v[98:113], v[126:129], v[190:193], v[98:113]
	s_setprio 0
	s_barrier
	v_cndmask_b32_e64 v64, 0, 1, s[40:41]
	v_cmp_ne_u32_e64 s[42:43], 1, v64
	s_andn2_b64 vcc, exec, s[40:41]
	s_mov_b64 s[2:3], -1
	s_cbranch_vccnz .LBB0_667
	s_nop 3
	v_exp_f32_e32 v64, v82
	v_exp_f32_e32 v65, v83
	v_exp_f32_e32 v66, v84
	v_exp_f32_e32 v67, v85
	v_exp_f32_e32 v68, v86
	v_exp_f32_e32 v69, v87
	v_exp_f32_e32 v70, v88
	v_exp_f32_e32 v71, v89
	v_exp_f32_e32 v72, v90
	v_exp_f32_e32 v73, v91
	v_exp_f32_e32 v74, v92
	v_exp_f32_e32 v75, v93
	v_exp_f32_e32 v76, v94
	v_exp_f32_e32 v77, v95
	v_exp_f32_e32 v78, v96
	s_cbranch_execz .LBB0_668

.LBB0_673:
	ds_read_b64_tr_b16 v[112:113], v231 offset:0
	ds_read_b64_tr_b16 v[114:115], v231 offset:0x800
	ds_read_b64_tr_b16 v[116:117], v231 offset:0x1000
	ds_read_b64_tr_b16 v[118:119], v231 offset:0x1800
	ds_read_b64_tr_b16 v[120:121], v231 offset:0x2000
	ds_read_b64_tr_b16 v[122:123], v231 offset:0x2800
	ds_read_b64_tr_b16 v[124:125], v231 offset:0x3000
	ds_read_b64_tr_b16 v[126:127], v231 offset:0x3800
	s_waitcnt lgkmcnt(0)
	s_nop 0
	s_setprio 1
	v_mfma_f32_32x32x16_bf16 v[0:15], v[96:99], v[112:115], v[0:15]
	ds_read_b64_tr_b16 v[112:113], v231 offset:0x200
	ds_read_b64_tr_b16 v[114:115], v231 offset:0xa00
	v_mfma_f32_32x32x16_bf16 v[0:15], v[100:103], v[116:119], v[0:15]
	ds_read_b64_tr_b16 v[116:117], v231 offset:0x1200
	ds_read_b64_tr_b16 v[118:119], v231 offset:0x1a00
	v_mfma_f32_32x32x16_bf16 v[0:15], v[104:107], v[120:123], v[0:15]
	ds_read_b64_tr_b16 v[120:121], v231 offset:0x2200
	ds_read_b64_tr_b16 v[122:123], v231 offset:0x2a00
	v_mfma_f32_32x32x16_bf16 v[0:15], v[108:111], v[124:127], v[0:15]
	ds_read_b64_tr_b16 v[124:125], v231 offset:0x3200
	ds_read_b64_tr_b16 v[126:127], v231 offset:0x3a00
	s_waitcnt lgkmcnt(0)
	v_mfma_f32_32x32x16_bf16 v[16:31], v[96:99], v[112:115], v[16:31]
	ds_read_b64_tr_b16 v[112:113], v231 offset:0x400
	ds_read_b64_tr_b16 v[114:115], v231 offset:0xc00
	v_mfma_f32_32x32x16_bf16 v[16:31], v[100:103], v[116:119], v[16:31]
	ds_read_b64_tr_b16 v[116:117], v231 offset:0x1400
	ds_read_b64_tr_b16 v[118:119], v231 offset:0x1c00
	v_mfma_f32_32x32x16_bf16 v[16:31], v[104:107], v[120:123], v[16:31]
	ds_read_b64_tr_b16 v[120:121], v231 offset:0x2400
	ds_read_b64_tr_b16 v[122:123], v231 offset:0x2c00
	v_mfma_f32_32x32x16_bf16 v[16:31], v[108:111], v[124:127], v[16:31]
	ds_read_b64_tr_b16 v[124:125], v231 offset:0x3400
	ds_read_b64_tr_b16 v[126:127], v231 offset:0x3c00
	s_waitcnt lgkmcnt(0)
	v_mfma_f32_32x32x16_bf16 v[32:47], v[96:99], v[112:115], v[32:47]
	ds_read_b64_tr_b16 v[112:113], v231 offset:0x600
	ds_read_b64_tr_b16 v[114:115], v231 offset:0xe00
	v_mfma_f32_32x32x16_bf16 v[32:47], v[100:103], v[116:119], v[32:47]
	ds_read_b64_tr_b16 v[116:117], v231 offset:0x1600
	ds_read_b64_tr_b16 v[118:119], v231 offset:0x1e00
	v_mfma_f32_32x32x16_bf16 v[32:47], v[104:107], v[120:123], v[32:47]
	ds_read_b64_tr_b16 v[120:121], v231 offset:0x2600
	ds_read_b64_tr_b16 v[122:123], v231 offset:0x2e00
	v_mfma_f32_32x32x16_bf16 v[32:47], v[108:111], v[124:127], v[32:47]
	ds_read_b64_tr_b16 v[124:125], v231 offset:0x3600
	ds_read_b64_tr_b16 v[126:127], v231 offset:0x3e00
	s_waitcnt lgkmcnt(0)
	v_mfma_f32_32x32x16_bf16 v[48:63], v[96:99], v[112:115], v[48:63]
	v_mfma_f32_32x32x16_bf16 v[48:63], v[100:103], v[116:119], v[48:63]
	v_mfma_f32_32x32x16_bf16 v[48:63], v[104:107], v[120:123], v[48:63]
	v_mfma_f32_32x32x16_bf16 v[48:63], v[108:111], v[124:127], v[48:63]
	ds_read_b128 v[96:99], v213 offset:49152
	ds_read_b128 v[100:103], v213 offset:57344
	ds_read_b128 v[104:107], v241 offset:49152
	ds_read_b128 v[108:111], v241 offset:57344
	ds_read_b128 v[144:147], v244 offset:49152
	ds_read_b128 v[148:151], v244 offset:57344
	ds_read_b128 v[152:155], v246 offset:49152
	ds_read_b128 v[156:159], v246 offset:57344
	s_waitcnt lgkmcnt(7)
	v_mfma_f32_32x32x16_bf16 v[112:127], v[96:99], v[162:165], 0
	s_waitcnt lgkmcnt(6)
	v_mfma_f32_32x32x16_bf16 v[128:143], v[100:103], v[162:165], 0
	s_waitcnt lgkmcnt(5)
	v_mfma_f32_32x32x16_bf16 v[112:127], v[104:107], v[166:169], v[112:127]
	s_waitcnt lgkmcnt(4)
	v_mfma_f32_32x32x16_bf16 v[128:143], v[108:111], v[166:169], v[128:143]
	s_waitcnt lgkmcnt(3)
	v_mfma_f32_32x32x16_bf16 v[112:127], v[144:147], v[170:173], v[112:127]
	s_waitcnt lgkmcnt(2)
	v_mfma_f32_32x32x16_bf16 v[128:143], v[148:151], v[170:173], v[128:143]
	s_waitcnt lgkmcnt(1)
	v_mfma_f32_32x32x16_bf16 v[112:127], v[152:155], v[174:177], v[112:127]
	s_waitcnt lgkmcnt(0)
	v_mfma_f32_32x32x16_bf16 v[128:143], v[156:159], v[174:177], v[128:143]
	ds_read_b128 v[96:99], v247 offset:49152
	ds_read_b128 v[100:103], v247 offset:57344
	ds_read_b128 v[104:107], v249 offset:49152
	ds_read_b128 v[108:111], v249 offset:57344
	ds_read_b128 v[144:147], v226 offset:49152
	ds_read_b128 v[148:151], v226 offset:57344
	ds_read_b128 v[152:155], v227 offset:49152
	ds_read_b128 v[156:159], v227 offset:57344
	s_waitcnt lgkmcnt(7)
	v_mfma_f32_32x32x16_bf16 v[112:127], v[96:99], v[178:181], v[112:127]
	s_waitcnt lgkmcnt(6)
	v_mfma_f32_32x32x16_bf16 v[128:143], v[100:103], v[178:181], v[128:143]
	s_waitcnt lgkmcnt(5)
	v_mfma_f32_32x32x16_bf16 v[112:127], v[104:107], v[182:185], v[112:127]
	s_waitcnt lgkmcnt(4)
	v_mfma_f32_32x32x16_bf16 v[128:143], v[108:111], v[182:185], v[128:143]
	s_waitcnt lgkmcnt(3)
	v_mfma_f32_32x32x16_bf16 v[112:127], v[144:147], v[186:189], v[112:127]
	s_waitcnt lgkmcnt(2)
	v_mfma_f32_32x32x16_bf16 v[128:143], v[148:151], v[186:189], v[128:143]
	s_waitcnt lgkmcnt(1)
	v_mfma_f32_32x32x16_bf16 v[112:127], v[152:155], v[190:193], v[112:127]
	s_waitcnt lgkmcnt(0)
	v_mfma_f32_32x32x16_bf16 v[128:143], v[156:159], v[190:193], v[128:143]
	s_setprio 0
	s_barrier
	s_and_b64 vcc, exec, s[42:43]
	s_mov_b64 s[2:3], -1
	s_cbranch_vccnz .LBB0_677
	s_nop 5
	v_exp_f32_e32 v96, v112
	v_exp_f32_e32 v97, v113
	v_exp_f32_e32 v98, v114
	v_exp_f32_e32 v99, v115
	v_exp_f32_e32 v100, v116
	v_exp_f32_e32 v101, v117
	v_exp_f32_e32 v102, v118
	v_exp_f32_e32 v103, v119
	v_exp_f32_e32 v104, v120
	v_exp_f32_e32 v105, v121
	v_exp_f32_e32 v106, v122
	v_exp_f32_e32 v107, v123
	v_exp_f32_e32 v108, v124
	v_exp_f32_e32 v109, v125
	v_exp_f32_e32 v110, v126
	s_cbranch_execz .LBB0_678

.LBB0_687:
	s_lshl_b64 s[2:3], s[2:3], 1
	s_add_u32 s2, s18, s2
	s_addc_u32 s3, s19, s3
	global_load_dwordx4 v[146:149], v210, s[2:3]
	global_load_dwordx4 v[150:153], v210, s[2:3] offset:256
	global_load_dwordx4 v[154:157], v212, s[2:3]
	global_load_dwordx4 v[194:197], v212, s[2:3] offset:256
	ds_read_b128 v[64:67], v204 offset:32768
	ds_read_b128 v[68:71], v204 offset:40960
	ds_read_b128 v[72:75], v205 offset:32768
	ds_read_b128 v[76:79], v205 offset:40960
	ds_read_b128 v[80:83], v206 offset:32768
	ds_read_b128 v[84:87], v206 offset:40960
	ds_read_b128 v[88:91], v207 offset:32768
	ds_read_b128 v[92:95], v207 offset:40960
	s_waitcnt lgkmcnt(7)
	s_setprio 1
	v_mfma_f32_32x32x16_bf16 v[112:127], v[64:67], v[162:165], 0
	s_waitcnt lgkmcnt(6)
	v_mfma_f32_32x32x16_bf16 v[96:111], v[68:71], v[162:165], 0
	s_waitcnt lgkmcnt(5)
	v_mfma_f32_32x32x16_bf16 v[112:127], v[72:75], v[166:169], v[112:127]
	s_waitcnt lgkmcnt(4)
	v_mfma_f32_32x32x16_bf16 v[96:111], v[76:79], v[166:169], v[96:111]
	s_waitcnt lgkmcnt(3)
	v_mfma_f32_32x32x16_bf16 v[112:127], v[80:83], v[170:173], v[112:127]
	s_waitcnt lgkmcnt(2)
	v_mfma_f32_32x32x16_bf16 v[96:111], v[84:87], v[170:173], v[96:111]
	s_waitcnt lgkmcnt(1)
	v_mfma_f32_32x32x16_bf16 v[112:127], v[88:91], v[174:177], v[112:127]
	s_waitcnt lgkmcnt(0)
	v_mfma_f32_32x32x16_bf16 v[96:111], v[92:95], v[174:177], v[96:111]
	ds_read_b128 v[64:67], v208 offset:32768
	ds_read_b128 v[68:71], v208 offset:40960
	ds_read_b128 v[72:75], v209 offset:32768
	ds_read_b128 v[76:79], v209 offset:40960
	ds_read_b128 v[80:83], v213 offset:32768
	ds_read_b128 v[84:87], v213 offset:40960
	ds_read_b128 v[88:91], v214 offset:32768
	ds_read_b128 v[92:95], v214 offset:40960
	s_waitcnt lgkmcnt(7)
	v_mfma_f32_32x32x16_bf16 v[112:127], v[64:67], v[178:181], v[112:127]
	s_waitcnt lgkmcnt(6)
	v_mfma_f32_32x32x16_bf16 v[96:111], v[68:71], v[178:181], v[96:111]
	s_waitcnt lgkmcnt(5)
	v_mfma_f32_32x32x16_bf16 v[112:127], v[72:75], v[182:185], v[112:127]
	s_waitcnt lgkmcnt(4)
	v_mfma_f32_32x32x16_bf16 v[96:111], v[76:79], v[182:185], v[96:111]
	s_waitcnt lgkmcnt(3)
	v_mfma_f32_32x32x16_bf16 v[112:127], v[80:83], v[186:189], v[112:127]
	s_waitcnt lgkmcnt(2)
	v_mfma_f32_32x32x16_bf16 v[96:111], v[84:87], v[186:189], v[96:111]
	s_waitcnt lgkmcnt(1)
	v_mfma_f32_32x32x16_bf16 v[112:127], v[88:91], v[190:193], v[112:127]
	s_waitcnt lgkmcnt(0)
	v_mfma_f32_32x32x16_bf16 v[96:111], v[92:95], v[190:193], v[96:111]
	s_setprio 0
	v_cndmask_b32_e64 v64, 0, 1, s[40:41]
	v_cmp_ne_u32_e64 s[42:43], 1, v64
	s_andn2_b64 vcc, exec, s[40:41]
	s_mov_b64 s[2:3], -1
	s_cbranch_vccnz .LBB0_691
	s_nop 4
	v_exp_f32_e32 v64, v112
	v_exp_f32_e32 v65, v113
	v_exp_f32_e32 v66, v114
	v_exp_f32_e32 v67, v115
	v_exp_f32_e32 v68, v116
	v_exp_f32_e32 v69, v117
	v_exp_f32_e32 v70, v118
	v_exp_f32_e32 v71, v119
	v_exp_f32_e32 v72, v120
	v_exp_f32_e32 v73, v121
	v_exp_f32_e32 v74, v122
	v_exp_f32_e32 v75, v123
	v_exp_f32_e32 v76, v124
	v_exp_f32_e32 v77, v125
	v_exp_f32_e32 v78, v126
	s_cbranch_execz .LBB0_692

.LBB0_695:
	v_exp_f32_e32 v79, v127
	v_exp_f32_e32 v95, v111
	v_cvt_pk_bf16_f32 v96, v64, v65
	v_cvt_pk_bf16_f32 v97, v66, v67
	v_cvt_pk_bf16_f32 v98, v68, v69
	v_cvt_pk_bf16_f32 v99, v70, v71
	v_cvt_pk_bf16_f32 v100, v72, v73
	v_cvt_pk_bf16_f32 v101, v74, v75
	v_cvt_pk_bf16_f32 v102, v76, v77
	v_cvt_pk_bf16_f32 v103, v78, v79
	v_cvt_pk_bf16_f32 v104, v80, v81
	v_cvt_pk_bf16_f32 v105, v82, v83
	v_cvt_pk_bf16_f32 v106, v84, v85
	v_cvt_pk_bf16_f32 v107, v86, v87
	v_cvt_pk_bf16_f32 v108, v88, v89
	v_cvt_pk_bf16_f32 v109, v90, v91
	v_cvt_pk_bf16_f32 v110, v92, v93
	v_cvt_pk_bf16_f32 v111, v94, v95
	v_permlane32_swap_b32_e32 v96, v98
	v_permlane32_swap_b32_e32 v97, v99
	v_permlane32_swap_b32_e32 v100, v102
	v_permlane32_swap_b32_e32 v101, v103
	v_permlane32_swap_b32_e32 v104, v106
	v_permlane32_swap_b32_e32 v105, v107
	v_permlane32_swap_b32_e32 v108, v110
	v_permlane32_swap_b32_e32 v109, v111
	s_barrier
	ds_read_b64_tr_b16 v[112:113], v231 offset:0
	ds_read_b64_tr_b16 v[114:115], v231 offset:0x800
	ds_read_b64_tr_b16 v[116:117], v231 offset:0x1000
	ds_read_b64_tr_b16 v[118:119], v231 offset:0x1800
	ds_read_b64_tr_b16 v[120:121], v231 offset:0x2000
	ds_read_b64_tr_b16 v[122:123], v231 offset:0x2800
	ds_read_b64_tr_b16 v[124:125], v231 offset:0x3000
	ds_read_b64_tr_b16 v[126:127], v231 offset:0x3800
	s_waitcnt lgkmcnt(0)
	s_nop 0
	s_setprio 1
	v_mfma_f32_32x32x16_bf16 v[0:15], v[96:99], v[112:115], v[0:15]
	ds_read_b64_tr_b16 v[112:113], v231 offset:0x200
	ds_read_b64_tr_b16 v[114:115], v231 offset:0xa00
	v_mfma_f32_32x32x16_bf16 v[0:15], v[100:103], v[116:119], v[0:15]
	ds_read_b64_tr_b16 v[116:117], v231 offset:0x1200
	ds_read_b64_tr_b16 v[118:119], v231 offset:0x1a00
	v_mfma_f32_32x32x16_bf16 v[0:15], v[104:107], v[120:123], v[0:15]
	ds_read_b64_tr_b16 v[120:121], v231 offset:0x2200
	ds_read_b64_tr_b16 v[122:123], v231 offset:0x2a00
	v_mfma_f32_32x32x16_bf16 v[0:15], v[108:111], v[124:127], v[0:15]
	ds_read_b64_tr_b16 v[124:125], v231 offset:0x3200
	ds_read_b64_tr_b16 v[126:127], v231 offset:0x3a00
	s_waitcnt lgkmcnt(0)
	v_mfma_f32_32x32x16_bf16 v[16:31], v[96:99], v[112:115], v[16:31]
	ds_read_b64_tr_b16 v[112:113], v231 offset:0x400
	ds_read_b64_tr_b16 v[114:115], v231 offset:0xc00
	v_mfma_f32_32x32x16_bf16 v[16:31], v[100:103], v[116:119], v[16:31]
	ds_read_b64_tr_b16 v[116:117], v231 offset:0x1400
	ds_read_b64_tr_b16 v[118:119], v231 offset:0x1c00
	v_mfma_f32_32x32x16_bf16 v[16:31], v[104:107], v[120:123], v[16:31]
	ds_read_b64_tr_b16 v[120:121], v231 offset:0x2400
	ds_read_b64_tr_b16 v[122:123], v231 offset:0x2c00
	v_mfma_f32_32x32x16_bf16 v[16:31], v[108:111], v[124:127], v[16:31]
	ds_read_b64_tr_b16 v[124:125], v231 offset:0x3400
	ds_read_b64_tr_b16 v[126:127], v231 offset:0x3c00
	s_waitcnt lgkmcnt(0)
	v_mfma_f32_32x32x16_bf16 v[32:47], v[96:99], v[112:115], v[32:47]
	ds_read_b64_tr_b16 v[112:113], v231 offset:0x600
	ds_read_b64_tr_b16 v[114:115], v231 offset:0xe00
	v_mfma_f32_32x32x16_bf16 v[32:47], v[100:103], v[116:119], v[32:47]
	ds_read_b64_tr_b16 v[116:117], v231 offset:0x1600
	ds_read_b64_tr_b16 v[118:119], v231 offset:0x1e00
	v_mfma_f32_32x32x16_bf16 v[32:47], v[104:107], v[120:123], v[32:47]
	ds_read_b64_tr_b16 v[120:121], v231 offset:0x2600
	ds_read_b64_tr_b16 v[122:123], v231 offset:0x2e00
	v_mfma_f32_32x32x16_bf16 v[32:47], v[108:111], v[124:127], v[32:47]
	ds_read_b64_tr_b16 v[124:125], v231 offset:0x3600
	ds_read_b64_tr_b16 v[126:127], v231 offset:0x3e00
	s_waitcnt lgkmcnt(0)
	v_mfma_f32_32x32x16_bf16 v[48:63], v[96:99], v[112:115], v[48:63]
	s_setprio 0
	s_waitcnt vmcnt(0)
	v_cndmask_b32_e64 v96, 0, 1, s[48:49]
	v_cmp_ne_u32_e64 s[44:45], 1, v96
	s_andn2_b64 vcc, exec, s[48:49]
	s_waitcnt vmcnt(3)
	ds_write_b128 v232, v[146:149] offset:49152
	s_waitcnt vmcnt(1)
	ds_write_b128 v233, v[154:157] offset:49152
	ds_write_b128 v234, v[150:153] offset:16384
	s_waitcnt vmcnt(0)
	ds_write_b128 v235, v[194:197] offset:16384
	s_waitcnt lgkmcnt(0)
	v_mfma_f32_32x32x16_bf16 v[48:63], v[100:103], v[116:119], v[48:63]
	s_barrier
	v_mfma_f32_32x32x16_bf16 v[48:63], v[104:107], v[120:123], v[48:63]
	v_mfma_f32_32x32x16_bf16 v[48:63], v[108:111], v[124:127], v[48:63]
	s_cbranch_vccnz .LBB0_697
	global_load_dwordx4 v[146:149], v[158:159], off
	global_load_dwordx4 v[154:157], v[198:199], off
	global_load_dwordx4 v[150:153], v[200:201], off
	global_load_dwordx4 v[194:197], v[202:203], off
.LBB0_697:
	ds_read_b128 v[96:99], v204 offset:49152
	ds_read_b128 v[100:103], v204 offset:57344
	ds_read_b128 v[104:107], v205 offset:49152
	ds_read_b128 v[108:111], v205 offset:57344
	ds_read_b128 v[216:219], v206 offset:49152
	ds_read_b128 v[226:229], v206 offset:57344
	ds_read_b128 v[236:239], v207 offset:49152
	ds_read_b128 v[246:249], v207 offset:57344
	s_waitcnt lgkmcnt(7)
	s_setprio 1
	v_mfma_f32_32x32x16_bf16 v[114:129], v[96:99], v[162:165], 0
	s_waitcnt lgkmcnt(6)
	v_mfma_f32_32x32x16_bf16 v[130:145], v[100:103], v[162:165], 0
	s_waitcnt lgkmcnt(5)
	v_mfma_f32_32x32x16_bf16 v[114:129], v[104:107], v[166:169], v[114:129]
	s_waitcnt lgkmcnt(4)
	v_mfma_f32_32x32x16_bf16 v[130:145], v[108:111], v[166:169], v[130:145]
	s_waitcnt lgkmcnt(3)
	v_mfma_f32_32x32x16_bf16 v[114:129], v[216:219], v[170:173], v[114:129]
	s_waitcnt lgkmcnt(2)
	v_mfma_f32_32x32x16_bf16 v[130:145], v[226:229], v[170:173], v[130:145]
	s_waitcnt lgkmcnt(1)
	v_mfma_f32_32x32x16_bf16 v[114:129], v[236:239], v[174:177], v[114:129]
	s_waitcnt lgkmcnt(0)
	v_mfma_f32_32x32x16_bf16 v[130:145], v[246:249], v[174:177], v[130:145]
	ds_read_b128 v[96:99], v208 offset:49152
	ds_read_b128 v[100:103], v208 offset:57344
	ds_read_b128 v[104:107], v209 offset:49152
	ds_read_b128 v[108:111], v209 offset:57344
	ds_read_b128 v[216:219], v213 offset:49152
	ds_read_b128 v[226:229], v213 offset:57344
	ds_read_b128 v[236:239], v214 offset:49152
	ds_read_b128 v[246:249], v214 offset:57344
	s_waitcnt lgkmcnt(7)
	v_mfma_f32_32x32x16_bf16 v[114:129], v[96:99], v[178:181], v[114:129]
	s_waitcnt lgkmcnt(6)
	v_mfma_f32_32x32x16_bf16 v[130:145], v[100:103], v[178:181], v[130:145]
	s_waitcnt lgkmcnt(5)
	v_mfma_f32_32x32x16_bf16 v[114:129], v[104:107], v[182:185], v[114:129]
	s_waitcnt lgkmcnt(4)
	v_mfma_f32_32x32x16_bf16 v[130:145], v[108:111], v[182:185], v[130:145]
	s_waitcnt lgkmcnt(3)
	v_mfma_f32_32x32x16_bf16 v[114:129], v[216:219], v[186:189], v[114:129]
	s_waitcnt lgkmcnt(2)
	v_mfma_f32_32x32x16_bf16 v[130:145], v[226:229], v[186:189], v[130:145]
	s_waitcnt lgkmcnt(1)
	v_mfma_f32_32x32x16_bf16 v[114:129], v[236:239], v[190:193], v[114:129]
	s_waitcnt lgkmcnt(0)
	v_mfma_f32_32x32x16_bf16 v[130:145], v[246:249], v[190:193], v[130:145]
	s_setprio 0
	s_and_b64 vcc, exec, s[42:43]
	s_mov_b64 s[2:3], -1
	s_cbranch_vccnz .LBB0_701
	s_nop 6
	v_exp_f32_e32 v96, v114
	v_exp_f32_e32 v97, v115
	v_exp_f32_e32 v98, v116
	v_exp_f32_e32 v99, v117
	v_exp_f32_e32 v100, v118
	v_exp_f32_e32 v101, v119
	v_exp_f32_e32 v102, v120
	v_exp_f32_e32 v103, v121
	v_exp_f32_e32 v104, v122
	v_exp_f32_e32 v105, v123
	v_exp_f32_e32 v106, v124
	v_exp_f32_e32 v107, v125
	v_exp_f32_e32 v108, v126
	v_exp_f32_e32 v109, v127
	v_exp_f32_e32 v110, v128
	s_cbranch_execz .LBB0_702

.LBB0_705:
	v_exp_f32_e32 v111, v129
	s_nop 0
	v_exp_f32_e32 v127, v145
	v_cvt_pk_bf16_f32 v128, v96, v97
	v_cvt_pk_bf16_f32 v129, v98, v99
	v_cvt_pk_bf16_f32 v130, v100, v101
	v_cvt_pk_bf16_f32 v131, v102, v103
	v_cvt_pk_bf16_f32 v132, v104, v105
	v_cvt_pk_bf16_f32 v133, v106, v107
	v_cvt_pk_bf16_f32 v134, v108, v109
	v_cvt_pk_bf16_f32 v135, v110, v111
	v_cvt_pk_bf16_f32 v136, v112, v113
	v_cvt_pk_bf16_f32 v137, v114, v115
	v_cvt_pk_bf16_f32 v138, v116, v117
	v_cvt_pk_bf16_f32 v139, v118, v119
	v_cvt_pk_bf16_f32 v140, v120, v121
	v_cvt_pk_bf16_f32 v141, v122, v123
	v_cvt_pk_bf16_f32 v142, v124, v125
	v_cvt_pk_bf16_f32 v143, v126, v127
	v_permlane32_swap_b32_e32 v128, v130
	v_permlane32_swap_b32_e32 v129, v131
	v_permlane32_swap_b32_e32 v132, v134
	v_permlane32_swap_b32_e32 v133, v135
	v_permlane32_swap_b32_e32 v136, v138
	v_permlane32_swap_b32_e32 v137, v139
	v_permlane32_swap_b32_e32 v140, v142
	v_permlane32_swap_b32_e32 v141, v143
	s_barrier
	ds_read_b64_tr_b16 v[216:217], v160 offset:0
	ds_read_b64_tr_b16 v[218:219], v160 offset:0x800
	ds_read_b64_tr_b16 v[226:227], v160 offset:0x1000
	ds_read_b64_tr_b16 v[228:229], v160 offset:0x1800
	ds_read_b64_tr_b16 v[236:237], v160 offset:0x2000
	ds_read_b64_tr_b16 v[238:239], v160 offset:0x2800
	ds_read_b64_tr_b16 v[246:247], v160 offset:0x3000
	ds_read_b64_tr_b16 v[248:249], v160 offset:0x3800
	s_waitcnt lgkmcnt(0)
	s_nop 0
	s_setprio 1
	v_mfma_f32_32x32x16_bf16 v[0:15], v[128:131], v[216:219], v[0:15]
	ds_read_b64_tr_b16 v[216:217], v160 offset:0x200
	ds_read_b64_tr_b16 v[218:219], v160 offset:0xa00
	v_mfma_f32_32x32x16_bf16 v[0:15], v[132:135], v[226:229], v[0:15]
	ds_read_b64_tr_b16 v[226:227], v160 offset:0x1200
	ds_read_b64_tr_b16 v[228:229], v160 offset:0x1a00
	v_mfma_f32_32x32x16_bf16 v[0:15], v[136:139], v[236:239], v[0:15]
	ds_read_b64_tr_b16 v[236:237], v160 offset:0x2200
	ds_read_b64_tr_b16 v[238:239], v160 offset:0x2a00
	v_mfma_f32_32x32x16_bf16 v[0:15], v[140:143], v[246:249], v[0:15]
	ds_read_b64_tr_b16 v[246:247], v160 offset:0x3200
	ds_read_b64_tr_b16 v[248:249], v160 offset:0x3a00
	s_waitcnt lgkmcnt(0)
	v_mfma_f32_32x32x16_bf16 v[16:31], v[128:131], v[216:219], v[16:31]
	ds_read_b64_tr_b16 v[216:217], v160 offset:0x400
	ds_read_b64_tr_b16 v[218:219], v160 offset:0xc00
	v_mfma_f32_32x32x16_bf16 v[16:31], v[132:135], v[226:229], v[16:31]
	ds_read_b64_tr_b16 v[226:227], v160 offset:0x1400
	ds_read_b64_tr_b16 v[228:229], v160 offset:0x1c00
	v_mfma_f32_32x32x16_bf16 v[16:31], v[136:139], v[236:239], v[16:31]
	ds_read_b64_tr_b16 v[236:237], v160 offset:0x2400
	ds_read_b64_tr_b16 v[238:239], v160 offset:0x2c00
	v_mfma_f32_32x32x16_bf16 v[16:31], v[140:143], v[246:249], v[16:31]
	ds_read_b64_tr_b16 v[246:247], v160 offset:0x3400
	ds_read_b64_tr_b16 v[248:249], v160 offset:0x3c00
	s_waitcnt lgkmcnt(0)
	v_mfma_f32_32x32x16_bf16 v[32:47], v[128:131], v[216:219], v[32:47]
	ds_read_b64_tr_b16 v[216:217], v160 offset:0x600
	ds_read_b64_tr_b16 v[218:219], v160 offset:0xe00
	v_mfma_f32_32x32x16_bf16 v[32:47], v[132:135], v[226:229], v[32:47]
	ds_read_b64_tr_b16 v[226:227], v160 offset:0x1600
	ds_read_b64_tr_b16 v[228:229], v160 offset:0x1e00
	v_mfma_f32_32x32x16_bf16 v[32:47], v[136:139], v[236:239], v[32:47]
	ds_read_b64_tr_b16 v[236:237], v160 offset:0x2600
	ds_read_b64_tr_b16 v[238:239], v160 offset:0x2e00
	v_mfma_f32_32x32x16_bf16 v[32:47], v[140:143], v[246:249], v[32:47]
	ds_read_b64_tr_b16 v[246:247], v160 offset:0x3600
	ds_read_b64_tr_b16 v[248:249], v160 offset:0x3e00
	s_waitcnt lgkmcnt(0)
	v_mfma_f32_32x32x16_bf16 v[48:63], v[128:131], v[216:219], v[48:63]
	s_and_b64 vcc, exec, s[44:45]
	v_mfma_f32_32x32x16_bf16 v[48:63], v[132:135], v[226:229], v[48:63]
	v_mfma_f32_32x32x16_bf16 v[48:63], v[136:139], v[236:239], v[48:63]
	v_mfma_f32_32x32x16_bf16 v[48:63], v[140:143], v[246:249], v[48:63]
	s_setprio 0
	s_cbranch_vccnz .LBB0_686
	s_waitcnt vmcnt(0)
	s_waitcnt vmcnt(3)
	ds_write_b128 v232, v[146:149] offset:32768
	s_waitcnt vmcnt(2)
	ds_write_b128 v233, v[154:157] offset:32768
	s_waitcnt vmcnt(1)
	ds_write_b128 v234, v[150:153]
	s_waitcnt vmcnt(0)
	ds_write_b128 v235, v[194:197]
	s_branch .LBB0_686
